# P4 MoBA gate: the 12 list appends of an item issue their atomics together, one wait, stores at the loop latch; P12 v gather offsets by full-rate 24-bit mad
# baseline (speedup 1.0000x reference)
; __device__ __forceinline__ void p4_moba_gate(Frame& F) {
;     ...
;     unsigned* CNT = (unsigned*)(F.ws + WS_CTL) + CW_MCNT; int* LIST = (int*)(F.ws + WS_MLIST);
;     const int g = F.lane >> 4, l15 = F.lane & 15;
;     for (int item = F.gw + 16 * MH; item < (S_ / 16) * MH; item += F.NGW) {
;         const int tile = item >> 4, h = item & 15, t0 = tile * 16, blk = t0 >> 8;
;         f32x4 acc[2] = {{0.f, 0.f, 0.f, 0.f}, {0.f, 0.f, 0.f, 0.f}};
; #pragma unroll
;         for (int ks = 0; ks < 4; ++ks) { const gbf16x8 a = *(const gbf16x8*)(ZM + (size_t)(t0 + l15) * ZM_LD + h * MD + 32 * ks + 8 * g);
; #pragma unroll
;             for (int nt = 0; nt < 2; ++nt) { const size_t o = ((size_t)h * MNB + l15 + 16 * nt) * MD + 32 * ks + 8 * g;
;                 acc[nt] = __builtin_amdgcn_mfma_f32_16x16x32_bf16(a, *(const gbf16x8*)(KMH + o), acc[nt], 0, 0, 0);
;                 acc[nt] = __builtin_amdgcn_mfma_f32_16x16x32_bf16(a, *(const gbf16x8*)(KML + o), acc[nt], 0, 0, 0); } }
; #pragma unroll
;         for (int r4 = 0; r4 < 4; ++r4) {
;             float s0 = l15 < blk ? acc[0][r4] : -INFINITY, s1 = l15 + 16 < blk ? acc[1][r4] : -INFINITY;
;             const int t = t0 + 4 * g + r4;
; #pragma unroll
;             for (int r = 0; r < 3; ++r) { const float m = dpp_max16(fmaxf(s0, s1));
;                 const int jm = (s0 == m) ? l15 : ((s1 == m) ? l15 + 16 : 99); const int jw = dpp_min16i(jm);
;                 if (m > -INFINITY && jm == jw) { const unsigned pos = atomicAdd(&CNT[(h * 32 + jw) * 16], 1u); LIST[(size_t)h * MLIST_HEAD + moba_list_off(jw) + pos] = t * 4 + r;
;                     if (jw < 16) s0 = -INFINITY; else s1 = -INFINITY; } }
;         }
.LBB0_1893:
	s_cmpk_lt_i32 s94, 0x1f00
	s_cbranch_scc0 .LBB0_1920
	s_add_u32 s0, s68, 0x2dc00000
	s_addc_u32 s1, s69, 0
	s_add_u32 s10, s68, 0x100000
	s_addc_u32 s11, s69, 0
	s_add_u32 s28, s68, 0x140000
	s_addc_u32 s29, s69, 0
	s_add_u32 s30, s68, 0x10000
	s_addc_u32 s31, s69, 0
	v_ashrrev_i32_e32 v2, 1, v124
	s_add_u32 s3, s68, 0x1700000
	v_and_b32_e32 v10, -8, v2
	s_addc_u32 s33, s69, 0
	s_add_i32 s35, s94, 0x100
	v_ashrrev_i32_e32 v11, 31, v10
	v_or_b32_e32 v16, 16, v1
	v_lshlrev_b32_e32 v17, 7, v1
	v_and_b32_e32 v18, -16, v124
	s_movk_i32 s42, 0x3000
	v_mov_b64_e32 v[12:13], s[0:1]
	s_mov_b32 s39, 0
	v_mov_b32_e32 v15, 0
	s_mov_b32 s43, 0xff800000
	v_mov_b32_e32 v19, 0xff800000
	v_mov_b32_e32 v20, 0x63
	v_mov_b32_e32 v21, 1
	v_mov_b32_e32 v22, 0x2000
	v_mov_b32_e32 v204, 0
	v_mov_b32_e32 v131, 0
	v_mov_b32_e32 v205, 0
	v_mov_b32_e32 v133, 0
	v_mov_b32_e32 v206, 0
	v_mov_b32_e32 v135, 0
	v_mov_b32_e32 v207, 0
	v_mov_b32_e32 v137, 0
	v_mov_b32_e32 v208, 0
	v_mov_b32_e32 v139, 0
	v_mov_b32_e32 v209, 0
	v_mov_b32_e32 v141, 0
	v_mov_b32_e32 v210, 0
	v_mov_b32_e32 v143, 0
	v_mov_b32_e32 v211, 0
	v_mov_b32_e32 v145, 0
	v_mov_b32_e32 v212, 0
	v_mov_b32_e32 v147, 0
	v_mov_b32_e32 v213, 0
	v_mov_b32_e32 v149, 0
	v_mov_b32_e32 v214, 0
	v_mov_b32_e32 v151, 0
	v_mov_b32_e32 v215, 0
	v_mov_b32_e32 v153, 0
	s_branch .LBB0_1896
.LBB0_1895:
	s_or_b64 exec, exec, s[0:1]
	s_waitcnt vmcnt(0)
	v_cmp_ne_u32_e32 vcc, 0, v204
	s_and_saveexec_b64 s[0:1], vcc
	v_lshl_add_u64 v[160:161], v[130:131], 2, v[160:161]
	global_store_dword v[160:161], v190, off
	v_mov_b32_e32 v204, 0
	s_or_b64 exec, exec, s[0:1]
	v_cmp_ne_u32_e32 vcc, 0, v205
	s_and_saveexec_b64 s[0:1], vcc
	v_lshl_add_u64 v[162:163], v[132:133], 2, v[162:163]
	global_store_dword v[162:163], v191, off
	v_mov_b32_e32 v205, 0
	s_or_b64 exec, exec, s[0:1]
	v_cmp_ne_u32_e32 vcc, 0, v206
	s_and_saveexec_b64 s[0:1], vcc
	v_lshl_add_u64 v[164:165], v[134:135], 2, v[164:165]
	global_store_dword v[164:165], v192, off
	v_mov_b32_e32 v206, 0
	s_or_b64 exec, exec, s[0:1]
	v_cmp_ne_u32_e32 vcc, 0, v207
	s_and_saveexec_b64 s[0:1], vcc
	v_lshl_add_u64 v[166:167], v[136:137], 2, v[166:167]
	global_store_dword v[166:167], v193, off
	v_mov_b32_e32 v207, 0
	s_or_b64 exec, exec, s[0:1]
	v_cmp_ne_u32_e32 vcc, 0, v208
	s_and_saveexec_b64 s[0:1], vcc
	v_lshl_add_u64 v[168:169], v[138:139], 2, v[168:169]
	global_store_dword v[168:169], v194, off
	v_mov_b32_e32 v208, 0
	s_or_b64 exec, exec, s[0:1]
	v_cmp_ne_u32_e32 vcc, 0, v209
	s_and_saveexec_b64 s[0:1], vcc
	v_lshl_add_u64 v[170:171], v[140:141], 2, v[170:171]
	global_store_dword v[170:171], v195, off
	v_mov_b32_e32 v209, 0
	s_or_b64 exec, exec, s[0:1]
	v_cmp_ne_u32_e32 vcc, 0, v210
	s_and_saveexec_b64 s[0:1], vcc
	v_lshl_add_u64 v[172:173], v[142:143], 2, v[172:173]
	global_store_dword v[172:173], v196, off
	v_mov_b32_e32 v210, 0
	s_or_b64 exec, exec, s[0:1]
	v_cmp_ne_u32_e32 vcc, 0, v211
	s_and_saveexec_b64 s[0:1], vcc
	v_lshl_add_u64 v[174:175], v[144:145], 2, v[174:175]
	global_store_dword v[174:175], v197, off
	v_mov_b32_e32 v211, 0
	s_or_b64 exec, exec, s[0:1]
	v_cmp_ne_u32_e32 vcc, 0, v212
	s_and_saveexec_b64 s[0:1], vcc
	v_lshl_add_u64 v[176:177], v[146:147], 2, v[176:177]
	global_store_dword v[176:177], v198, off
	v_mov_b32_e32 v212, 0
	s_or_b64 exec, exec, s[0:1]
	v_cmp_ne_u32_e32 vcc, 0, v213
	s_and_saveexec_b64 s[0:1], vcc
	v_lshl_add_u64 v[178:179], v[148:149], 2, v[178:179]
	global_store_dword v[178:179], v199, off
	v_mov_b32_e32 v213, 0
	s_or_b64 exec, exec, s[0:1]
	v_cmp_ne_u32_e32 vcc, 0, v214
	s_and_saveexec_b64 s[0:1], vcc
	v_lshl_add_u64 v[180:181], v[150:151], 2, v[180:181]
	global_store_dword v[180:181], v200, off
	v_mov_b32_e32 v214, 0
	s_or_b64 exec, exec, s[0:1]
	v_cmp_ne_u32_e32 vcc, 0, v215
	s_and_saveexec_b64 s[0:1], vcc
	v_lshl_add_u64 v[182:183], v[152:153], 2, v[182:183]
	global_store_dword v[182:183], v201, off
	v_mov_b32_e32 v215, 0
	s_or_b64 exec, exec, s[0:1]
	s_add_i32 s35, s35, s34
	s_cmpk_lt_i32 s35, 0x2000
	s_cbranch_scc0 .LBB0_1920
.LBB0_1896:
	s_and_b32 s5, s35, -16
	s_and_b32 s4, s35, 15
	v_or_b32_e32 v2, s5, v1
	v_mad_i64_i32 v[2:3], s[0:1], v2, s42, v[12:13]
	s_lshl_b32 s38, s4, 8
	v_lshl_add_u64 v[2:3], v[2:3], 0, s[38:39]
	v_lshl_add_u64 v[60:61], v[10:11], 1, v[2:3]
	v_lshl_or_b32 v14, s4, 12, v17
	global_load_dwordx4 v[2:5], v[60:61], off
	v_lshl_add_u64 v[6:7], v[14:15], 0, v[10:11]
	v_lshlrev_b64 v[24:25], 1, v[6:7]
	v_lshl_add_u64 v[6:7], s[10:11], 0, v[24:25]
	global_load_dwordx4 v[6:9], v[6:7], off
	v_lshl_add_u64 v[28:29], s[28:29], 0, v[24:25]
	v_or_b32_e32 v24, 0x800, v14
	v_mov_b32_e32 v25, v15
	v_lshl_add_u64 v[24:25], v[24:25], 0, v[10:11]
	v_lshlrev_b64 v[32:33], 1, v[24:25]
	v_lshl_add_u64 v[24:25], s[10:11], 0, v[32:33]
	global_load_dwordx4 v[24:27], v[24:25], off
	s_nop 0
	global_load_dwordx4 v[28:31], v[28:29], off
	v_lshl_add_u64 v[32:33], s[28:29], 0, v[32:33]
	global_load_dwordx4 v[32:35], v[32:33], off
	s_nop 0
	global_load_dwordx4 v[36:39], v[60:61], off offset:64
	v_or_b32_e32 v40, 32, v14
	v_mov_b32_e32 v41, v15
	v_lshl_add_u64 v[40:41], v[40:41], 0, v[10:11]
	v_lshlrev_b64 v[48:49], 1, v[40:41]
	v_lshl_add_u64 v[40:41], s[10:11], 0, v[48:49]
	global_load_dwordx4 v[40:43], v[40:41], off
	v_or_b32_e32 v44, 0x820, v14
	v_mov_b32_e32 v45, v15
	v_lshl_add_u64 v[44:45], v[44:45], 0, v[10:11]
	v_lshlrev_b64 v[52:53], 1, v[44:45]
	v_lshl_add_u64 v[44:45], s[10:11], 0, v[52:53]
	v_mov_b32_e32 v51, v15
	v_mov_b32_e32 v55, v15
	v_or_b32_e32 v50, 64, v14
	v_or_b32_e32 v54, 0x840, v14
	v_lshl_add_u64 v[48:49], s[28:29], 0, v[48:49]
	global_load_dwordx4 v[44:47], v[44:45], off
	v_lshl_add_u64 v[62:63], v[50:51], 0, v[10:11]
	v_lshl_add_u64 v[64:65], v[54:55], 0, v[10:11]
	global_load_dwordx4 v[48:51], v[48:49], off
	v_lshl_add_u64 v[56:57], s[28:29], 0, v[52:53]
	global_load_dwordx4 v[52:55], v[60:61], off offset:128
	v_lshlrev_b64 v[62:63], 1, v[62:63]
	v_lshl_add_u64 v[66:67], s[10:11], 0, v[62:63]
	global_load_dwordx4 v[56:59], v[56:57], off
	v_lshlrev_b64 v[64:65], 1, v[64:65]
	s_ashr_i32 s0, s35, 8
	v_cmp_gt_i32_e32 vcc, s0, v1
	v_cmp_gt_i32_e64 s[0:1], s0, v16
	s_lshl_b32 s38, s4, 9
	s_mul_i32 s4, s4, 0x7c000
	v_lshl_add_u32 v23, s5, 2, v18
	s_add_u32 s40, s3, s4
	s_addc_u32 s41, s33, 0
	s_waitcnt vmcnt(9)
; __device__ __forceinline__ void p4_moba_gate(Frame& F) {
;     ...
;         for (int ks = 0; ks < 4; ++ks) { const gbf16x8 a = *(const gbf16x8*)(ZM + (size_t)(t0 + l15) * ZM_LD + h * MD + 32 * ks + 8 * g);
; #pragma unroll
;             for (int nt = 0; nt < 2; ++nt) { const size_t o = ((size_t)h * MNB + l15 + 16 * nt) * MD + 32 * ks + 8 * g;
;                 acc[nt] = __builtin_amdgcn_mfma_f32_16x16x32_bf16(a, *(const gbf16x8*)(KMH + o), acc[nt], 0, 0, 0);
;                 acc[nt] = __builtin_amdgcn_mfma_f32_16x16x32_bf16(a, *(const gbf16x8*)(KML + o), acc[nt], 0, 0, 0); } }
; #pragma unroll
;         for (int r4 = 0; r4 < 4; ++r4) {
;             float s0 = l15 < blk ? acc[0][r4] : -INFINITY, s1 = l15 + 16 < blk ? acc[1][r4] : -INFINITY;
;             const int t = t0 + 4 * g + r4;
; #pragma unroll
;             for (int r = 0; r < 3; ++r) { const float m = dpp_max16(fmaxf(s0, s1));
;                 const int jm = (s0 == m) ? l15 : ((s1 == m) ? l15 + 16 : 99); const int jw = dpp_min16i(jm);
;                 if (m > -INFINITY && jm == jw) { const unsigned pos = atomicAdd(&CNT[(h * 32 + jw) * 16], 1u); LIST[(size_t)h * MLIST_HEAD + moba_list_off(jw) + pos] = t * 4 + r;
;                     if (jw < 16) s0 = -INFINITY; else s1 = -INFINITY; } }
;         }
	v_mfma_f32_16x16x32_bf16 v[6:9], v[2:5], v[6:9], 0
	s_waitcnt vmcnt(8)
	v_mfma_f32_16x16x32_bf16 v[24:27], v[2:5], v[24:27], 0
	s_waitcnt vmcnt(7)
	v_mfma_f32_16x16x32_bf16 v[6:9], v[2:5], v[28:31], v[6:9]
	global_load_dwordx4 v[28:31], v[66:67], off
	v_lshl_add_u64 v[66:67], s[10:11], 0, v[64:65]
	s_waitcnt vmcnt(7)
	v_mfma_f32_16x16x32_bf16 v[2:5], v[2:5], v[32:35], v[24:27]
	v_lshl_add_u64 v[32:33], s[28:29], 0, v[62:63]
	global_load_dwordx4 v[32:35], v[32:33], off
	s_nop 0
	global_load_dwordx4 v[24:27], v[66:67], off
	s_waitcnt vmcnt(7)
	v_mfma_f32_16x16x32_bf16 v[6:9], v[36:39], v[40:43], v[6:9]
	v_lshl_add_u64 v[40:41], s[28:29], 0, v[64:65]
	global_load_dwordx4 v[40:43], v[40:41], off
	s_waitcnt vmcnt(7)
	v_mfma_f32_16x16x32_bf16 v[2:5], v[36:39], v[44:47], v[2:5]
	v_mov_b32_e32 v45, v15
	v_or_b32_e32 v44, 0x60, v14
	v_or_b32_e32 v14, 0x860, v14
	s_waitcnt vmcnt(6)
	v_mfma_f32_16x16x32_bf16 v[6:9], v[36:39], v[48:51], v[6:9]
	v_lshl_add_u64 v[44:45], v[44:45], 0, v[10:11]
	v_lshl_add_u64 v[46:47], v[14:15], 0, v[10:11]
	v_lshlrev_b64 v[44:45], 1, v[44:45]
	s_waitcnt vmcnt(4)
	v_mfma_f32_16x16x32_bf16 v[2:5], v[36:39], v[56:59], v[2:5]
	global_load_dwordx4 v[36:39], v[60:61], off offset:192
	v_lshl_add_u64 v[48:49], s[10:11], 0, v[44:45]
	v_lshlrev_b64 v[46:47], 1, v[46:47]
	v_lshl_add_u64 v[44:45], s[28:29], 0, v[44:45]
	s_waitcnt vmcnt(4)
	v_mfma_f32_16x16x32_bf16 v[6:9], v[52:55], v[28:31], v[6:9]
	global_load_dwordx4 v[28:31], v[48:49], off
	s_waitcnt vmcnt(4)
	v_mfma_f32_16x16x32_bf16 v[6:9], v[52:55], v[32:35], v[6:9]
	global_load_dwordx4 v[32:35], v[44:45], off
	v_lshl_add_u64 v[48:49], s[10:11], 0, v[46:47]
	v_lshl_add_u64 v[44:45], s[28:29], 0, v[46:47]
	s_waitcnt vmcnt(4)
	v_mfma_f32_16x16x32_bf16 v[2:5], v[52:55], v[24:27], v[2:5]
	global_load_dwordx4 v[24:27], v[48:49], off
	s_waitcnt vmcnt(4)
	v_mfma_f32_16x16x32_bf16 v[2:5], v[52:55], v[40:43], v[2:5]
	global_load_dwordx4 v[40:43], v[44:45], off
	s_waitcnt vmcnt(3)
	v_mfma_f32_16x16x32_bf16 v[6:9], v[36:39], v[28:31], v[6:9]
	v_mov_b32_e32 v28, v15
	v_mov_b32_e32 v29, v15
	v_mov_b32_e32 v30, v15
	s_waitcnt vmcnt(1)
	v_mfma_f32_16x16x32_bf16 v[24:27], v[36:39], v[24:27], v[2:5]
	v_mov_b32_e32 v31, v15
	v_mfma_f32_16x16x32_bf16 v[2:5], v[36:39], v[32:35], v[6:9]
	s_waitcnt vmcnt(0)
	v_mfma_f32_16x16x32_bf16 v[6:9], v[36:39], v[40:43], v[24:27]
	s_nop 5
	v_cndmask_b32_e32 v2, v19, v2, vcc
	s_nop 0
	v_cndmask_b32_e64 v6, v19, v6, s[0:1]
	v_max_f32_e32 v14, v2, v2
	v_max_f32_e32 v24, v6, v6
	v_max_f32_e32 v14, v14, v24
	s_nop 1
	v_mov_b32_dpp v28, v14 quad_perm:[1,0,3,2] row_mask:0xf bank_mask:0xf
	v_max_f32_e32 v24, v28, v28
	v_max_f32_e32 v24, v14, v24
	s_nop 1
	v_mov_b32_dpp v29, v24 quad_perm:[2,3,0,1] row_mask:0xf bank_mask:0xf
	v_max_f32_e32 v25, v29, v29
	v_max_f32_e32 v24, v24, v25
	s_nop 1
	v_mov_b32_dpp v30, v24 row_half_mirror row_mask:0xf bank_mask:0xf
	v_max_f32_e32 v25, v30, v30
	v_max_f32_e32 v24, v24, v25
	s_nop 1
	v_mov_b32_dpp v31, v24 row_mirror row_mask:0xf bank_mask:0xf
	v_max_f32_e32 v25, v31, v31
	v_max_f32_e32 v25, v24, v25
	v_cmp_eq_f32_e64 s[4:5], v6, v25
	v_cmp_lg_f32_e64 s[6:7], s43, v25
	s_nop 0
	v_cndmask_b32_e64 v24, v20, v16, s[4:5]
	v_cmp_eq_f32_e64 s[4:5], v2, v25
	s_nop 1
	v_cndmask_b32_e64 v24, v24, v1, s[4:5]
	s_nop 1
	v_min_i32_dpp v26, v24, v24 quad_perm:[1,0,3,2] row_mask:0xf bank_mask:0xf bound_ctrl:1
	s_nop 1
	v_min_i32_dpp v26, v26, v26 quad_perm:[2,3,0,1] row_mask:0xf bank_mask:0xf bound_ctrl:1
	s_nop 1
	v_min_i32_dpp v26, v26, v26 row_half_mirror row_mask:0xf bank_mask:0xf bound_ctrl:1
	s_nop 1
	v_min_i32_dpp v26, v26, v26 row_mirror row_mask:0xf bank_mask:0xf bound_ctrl:1
	v_cmp_eq_u32_e64 s[8:9], v24, v26
	s_and_b64 s[8:9], s[6:7], s[8:9]
	s_and_saveexec_b64 s[6:7], s[8:9]
	s_cbranch_execz .LBB0_1898
	v_lshlrev_b32_e32 v14, 4, v24
	v_add_lshl_u32 v14, v14, s38, 2
	global_atomic_add v130, v14, v21, s[30:31] sc0
	v_not_b32_e32 v25, v24
	v_lshl_add_u32 v25, v25, 7, v22
	v_mul_i32_i24_e32 v24, v25, v24
	v_cndmask_b32_e64 v2, v2, v19, s[4:5]
	v_cndmask_b32_e64 v6, v19, v6, s[4:5]
	v_ashrrev_i32_e32 v25, 31, v24
	v_max_f32_e32 v26, v6, v6
	v_max_f32_e32 v27, v2, v2
	v_lshl_add_u64 v[24:25], v[24:25], 2, s[40:41]
	v_mov_b32_e32 v160, v24
	v_mov_b32_e32 v161, v25
	v_max_f32_e32 v14, v27, v26
	v_mov_b32_e32 v190, v23
	v_mov_b32_e32 v204, 1
.LBB0_1898:
	s_or_b64 exec, exec, s[6:7]
	v_mov_b32_e32 v24, v15
	v_max_f32_e32 v25, v14, v14
	s_nop 0
	v_mov_b32_dpp v24, v14 quad_perm:[1,0,3,2] row_mask:0xf bank_mask:0xf
	v_max_f32_e32 v24, v24, v24
	v_max_f32_e32 v24, v25, v24
	v_mov_b32_e32 v25, v15
	s_nop 1
	v_mov_b32_dpp v25, v24 quad_perm:[2,3,0,1] row_mask:0xf bank_mask:0xf
	v_max_f32_e32 v25, v25, v25
	v_max_f32_e32 v24, v24, v25
	v_mov_b32_e32 v25, v15
	s_nop 1
	v_mov_b32_dpp v25, v24 row_half_mirror row_mask:0xf bank_mask:0xf
	v_max_f32_e32 v25, v25, v25
	v_max_f32_e32 v24, v24, v25
	v_mov_b32_e32 v25, v15
	s_nop 1
	v_mov_b32_dpp v25, v24 row_mirror row_mask:0xf bank_mask:0xf
	v_max_f32_e32 v25, v25, v25
	v_max_f32_e32 v25, v24, v25
	v_cmp_eq_f32_e64 s[4:5], v6, v25
	v_cmp_lg_f32_e64 s[6:7], s43, v25
	s_nop 0
	v_cndmask_b32_e64 v24, v20, v16, s[4:5]
	v_cmp_eq_f32_e64 s[4:5], v2, v25
	s_nop 1
	v_cndmask_b32_e64 v24, v24, v1, s[4:5]
	s_nop 1
	v_min_i32_dpp v26, v24, v24 quad_perm:[1,0,3,2] row_mask:0xf bank_mask:0xf bound_ctrl:1
	s_nop 1
	v_min_i32_dpp v26, v26, v26 quad_perm:[2,3,0,1] row_mask:0xf bank_mask:0xf bound_ctrl:1
	s_nop 1
	v_min_i32_dpp v26, v26, v26 row_half_mirror row_mask:0xf bank_mask:0xf bound_ctrl:1
	s_nop 1
	v_min_i32_dpp v26, v26, v26 row_mirror row_mask:0xf bank_mask:0xf bound_ctrl:1
	v_cmp_eq_u32_e64 s[8:9], v24, v26
	s_and_b64 s[8:9], s[6:7], s[8:9]
	s_and_saveexec_b64 s[6:7], s[8:9]
	s_cbranch_execz .LBB0_1900
	v_lshlrev_b32_e32 v14, 4, v24
	v_add_lshl_u32 v14, v14, s38, 2
	global_atomic_add v132, v14, v21, s[30:31] sc0
	v_not_b32_e32 v25, v24
	v_lshl_add_u32 v25, v25, 7, v22
	v_mul_i32_i24_e32 v24, v25, v24
	v_cndmask_b32_e64 v2, v2, v19, s[4:5]
	v_cndmask_b32_e64 v6, v19, v6, s[4:5]
	v_ashrrev_i32_e32 v25, 31, v24
	v_max_f32_e32 v27, v6, v6
	v_max_f32_e32 v28, v2, v2
	v_lshl_add_u64 v[24:25], v[24:25], 2, s[40:41]
	v_or_b32_e32 v26, 1, v23
	v_mov_b32_e32 v162, v24
	v_mov_b32_e32 v163, v25
	v_max_f32_e32 v14, v28, v27
	v_mov_b32_e32 v191, v26
	v_mov_b32_e32 v205, 1
; __device__ __forceinline__ void p4_moba_gate(Frame& F) {
;     ...
;         for (int r4 = 0; r4 < 4; ++r4) {
;             float s0 = l15 < blk ? acc[0][r4] : -INFINITY, s1 = l15 + 16 < blk ? acc[1][r4] : -INFINITY;
;             const int t = t0 + 4 * g + r4;
; #pragma unroll
;             for (int r = 0; r < 3; ++r) { const float m = dpp_max16(fmaxf(s0, s1));
;                 const int jm = (s0 == m) ? l15 : ((s1 == m) ? l15 + 16 : 99); const int jw = dpp_min16i(jm);
;                 if (m > -INFINITY && jm == jw) { const unsigned pos = atomicAdd(&CNT[(h * 32 + jw) * 16], 1u); LIST[(size_t)h * MLIST_HEAD + moba_list_off(jw) + pos] = t * 4 + r;
;                     if (jw < 16) s0 = -INFINITY; else s1 = -INFINITY; } }
;         }
.LBB0_1900:
	s_or_b64 exec, exec, s[6:7]
	v_mov_b32_e32 v24, v15
	s_nop 1
	v_mov_b32_dpp v24, v14 quad_perm:[1,0,3,2] row_mask:0xf bank_mask:0xf
	v_max_f32_e32 v24, v24, v24
	v_max_f32_e32 v14, v14, v14
	v_max_f32_e32 v14, v14, v24
	v_mov_b32_e32 v24, v15
	s_nop 1
	v_mov_b32_dpp v24, v14 quad_perm:[2,3,0,1] row_mask:0xf bank_mask:0xf
	v_max_f32_e32 v24, v24, v24
	v_max_f32_e32 v14, v14, v24
	v_mov_b32_e32 v24, v15
	s_nop 1
	v_mov_b32_dpp v24, v14 row_half_mirror row_mask:0xf bank_mask:0xf
	v_max_f32_e32 v24, v24, v24
	v_max_f32_e32 v14, v14, v24
	v_mov_b32_e32 v24, v15
	s_nop 1
	v_mov_b32_dpp v24, v14 row_mirror row_mask:0xf bank_mask:0xf
	v_max_f32_e32 v24, v24, v24
	v_max_f32_e32 v14, v14, v24
	v_cmp_eq_f32_e64 s[4:5], v6, v14
	s_nop 1
	v_cndmask_b32_e64 v6, v20, v16, s[4:5]
	v_cmp_eq_f32_e64 s[4:5], v2, v14
	s_nop 1
	v_cndmask_b32_e64 v2, v6, v1, s[4:5]
	v_cmp_lg_f32_e64 s[4:5], s43, v14
	s_nop 0
	v_min_i32_dpp v6, v2, v2 quad_perm:[1,0,3,2] row_mask:0xf bank_mask:0xf bound_ctrl:1
	s_nop 1
	v_min_i32_dpp v6, v6, v6 quad_perm:[2,3,0,1] row_mask:0xf bank_mask:0xf bound_ctrl:1
	s_nop 1
	v_min_i32_dpp v6, v6, v6 row_half_mirror row_mask:0xf bank_mask:0xf bound_ctrl:1
	s_nop 1
	v_min_i32_dpp v6, v6, v6 row_mirror row_mask:0xf bank_mask:0xf bound_ctrl:1
	v_cmp_eq_u32_e64 s[6:7], v2, v6
	s_and_b64 s[6:7], s[4:5], s[6:7]
	s_and_saveexec_b64 s[4:5], s[6:7]
	s_cbranch_execz .LBB0_1902
	v_lshlrev_b32_e32 v6, 4, v2
	v_add_lshl_u32 v6, v6, s38, 2
	global_atomic_add v134, v6, v21, s[30:31] sc0
	v_not_b32_e32 v24, v2
	v_lshl_add_u32 v24, v24, 7, v22
	v_mul_i32_i24_e32 v24, v24, v2
	v_ashrrev_i32_e32 v25, 31, v24
	v_lshl_add_u64 v[24:25], v[24:25], 2, s[40:41]
	v_or_b32_e32 v6, 2, v23
	v_mov_b32_e32 v164, v24
	v_mov_b32_e32 v165, v25
	v_mov_b32_e32 v192, v6
	v_mov_b32_e32 v206, 1
.LBB0_1902:
	s_or_b64 exec, exec, s[4:5]
	v_cndmask_b32_e32 v2, v19, v3, vcc
	v_cndmask_b32_e64 v3, v19, v7, s[0:1]
	v_max_f32_e32 v6, v3, v3
	v_max_f32_e32 v7, v2, v2
	v_max_f32_e32 v6, v7, v6
	v_mov_b32_e32 v7, v15
	v_mov_b32_e32 v14, v15
	s_nop 0
	v_mov_b32_dpp v7, v6 quad_perm:[1,0,3,2] row_mask:0xf bank_mask:0xf
	v_max_f32_e32 v7, v7, v7
	v_max_f32_e32 v7, v6, v7
	s_nop 1
	v_mov_b32_dpp v14, v7 quad_perm:[2,3,0,1] row_mask:0xf bank_mask:0xf
	v_max_f32_e32 v14, v14, v14
	v_max_f32_e32 v7, v7, v14
	v_mov_b32_e32 v14, v15
	s_nop 1
	v_mov_b32_dpp v14, v7 row_half_mirror row_mask:0xf bank_mask:0xf
	v_max_f32_e32 v14, v14, v14
	v_max_f32_e32 v7, v7, v14
	v_mov_b32_e32 v14, v15
	s_nop 1
	v_mov_b32_dpp v14, v7 row_mirror row_mask:0xf bank_mask:0xf
	v_max_f32_e32 v14, v14, v14
	v_max_f32_e32 v14, v7, v14
	v_cmp_eq_f32_e64 s[4:5], v3, v14
	v_cmp_lg_f32_e64 s[6:7], s43, v14
	s_nop 0
	v_cndmask_b32_e64 v7, v20, v16, s[4:5]
	v_cmp_eq_f32_e64 s[4:5], v2, v14
	s_nop 1
	v_cndmask_b32_e64 v7, v7, v1, s[4:5]
	s_nop 1
	v_min_i32_dpp v24, v7, v7 quad_perm:[1,0,3,2] row_mask:0xf bank_mask:0xf bound_ctrl:1
	s_nop 1
	v_min_i32_dpp v24, v24, v24 quad_perm:[2,3,0,1] row_mask:0xf bank_mask:0xf bound_ctrl:1
	s_nop 1
	v_min_i32_dpp v24, v24, v24 row_half_mirror row_mask:0xf bank_mask:0xf bound_ctrl:1
	s_nop 1
	v_min_i32_dpp v24, v24, v24 row_mirror row_mask:0xf bank_mask:0xf bound_ctrl:1
	v_cmp_eq_u32_e64 s[8:9], v7, v24
	s_and_b64 s[8:9], s[6:7], s[8:9]
	s_and_saveexec_b64 s[6:7], s[8:9]
	s_cbranch_execz .LBB0_1904
	v_lshlrev_b32_e32 v6, 4, v7
	v_add_lshl_u32 v6, v6, s38, 2
	global_atomic_add v136, v6, v21, s[30:31] sc0
	v_not_b32_e32 v6, v7
	v_lshl_add_u32 v6, v6, 7, v22
	v_mul_i32_i24_e32 v6, v6, v7
	v_ashrrev_i32_e32 v7, 31, v6
	v_cndmask_b32_e64 v2, v2, v19, s[4:5]
	v_cndmask_b32_e64 v3, v19, v3, s[4:5]
	v_lshl_add_u64 v[6:7], v[6:7], 2, s[40:41]
	v_or_b32_e32 v24, 4, v23
	v_max_f32_e32 v25, v3, v3
	v_max_f32_e32 v26, v2, v2
	v_mov_b32_e32 v166, v6
	v_mov_b32_e32 v167, v7
	v_mov_b32_e32 v193, v24
	v_mov_b32_e32 v207, 1
	v_max_f32_e32 v6, v26, v25
.LBB0_1904:
	s_or_b64 exec, exec, s[6:7]
	v_mov_b32_e32 v7, v15
	v_max_f32_e32 v14, v6, v6
	s_nop 0
	v_mov_b32_dpp v7, v6 quad_perm:[1,0,3,2] row_mask:0xf bank_mask:0xf
	v_max_f32_e32 v7, v7, v7
	v_max_f32_e32 v7, v14, v7
	v_mov_b32_e32 v14, v15
	s_nop 1
	v_mov_b32_dpp v14, v7 quad_perm:[2,3,0,1] row_mask:0xf bank_mask:0xf
	v_max_f32_e32 v14, v14, v14
	v_max_f32_e32 v7, v7, v14
	v_mov_b32_e32 v14, v15
	s_nop 1
	v_mov_b32_dpp v14, v7 row_half_mirror row_mask:0xf bank_mask:0xf
	v_max_f32_e32 v14, v14, v14
	v_max_f32_e32 v7, v7, v14
	v_mov_b32_e32 v14, v15
	s_nop 1
	v_mov_b32_dpp v14, v7 row_mirror row_mask:0xf bank_mask:0xf
	v_max_f32_e32 v14, v14, v14
	v_max_f32_e32 v14, v7, v14
	v_cmp_eq_f32_e64 s[4:5], v3, v14
	v_cmp_lg_f32_e64 s[6:7], s43, v14
	s_nop 0
	v_cndmask_b32_e64 v7, v20, v16, s[4:5]
	v_cmp_eq_f32_e64 s[4:5], v2, v14
	s_nop 1
	v_cndmask_b32_e64 v7, v7, v1, s[4:5]
	s_nop 1
	v_min_i32_dpp v24, v7, v7 quad_perm:[1,0,3,2] row_mask:0xf bank_mask:0xf bound_ctrl:1
	s_nop 1
	v_min_i32_dpp v24, v24, v24 quad_perm:[2,3,0,1] row_mask:0xf bank_mask:0xf bound_ctrl:1
	s_nop 1
	v_min_i32_dpp v24, v24, v24 row_half_mirror row_mask:0xf bank_mask:0xf bound_ctrl:1
	s_nop 1
	v_min_i32_dpp v24, v24, v24 row_mirror row_mask:0xf bank_mask:0xf bound_ctrl:1
	v_cmp_eq_u32_e64 s[8:9], v7, v24
	s_and_b64 s[8:9], s[6:7], s[8:9]
	s_and_saveexec_b64 s[6:7], s[8:9]
	s_cbranch_execz .LBB0_1906
	v_lshlrev_b32_e32 v6, 4, v7
	v_add_lshl_u32 v6, v6, s38, 2
	global_atomic_add v138, v6, v21, s[30:31] sc0
	v_not_b32_e32 v6, v7
	v_lshl_add_u32 v6, v6, 7, v22
	v_mul_i32_i24_e32 v6, v6, v7
	v_ashrrev_i32_e32 v7, 31, v6
	v_cndmask_b32_e64 v2, v2, v19, s[4:5]
	v_cndmask_b32_e64 v3, v19, v3, s[4:5]
	v_lshl_add_u64 v[6:7], v[6:7], 2, s[40:41]
	v_or_b32_e32 v24, 5, v23
	v_max_f32_e32 v25, v3, v3
	v_max_f32_e32 v26, v2, v2
	v_mov_b32_e32 v168, v6
	v_mov_b32_e32 v169, v7
	v_mov_b32_e32 v194, v24
	v_mov_b32_e32 v208, 1
	v_max_f32_e32 v6, v26, v25
; __device__ __forceinline__ void p4_moba_gate(Frame& F) {
;     ...
;         for (int r4 = 0; r4 < 4; ++r4) {
;             float s0 = l15 < blk ? acc[0][r4] : -INFINITY, s1 = l15 + 16 < blk ? acc[1][r4] : -INFINITY;
;             const int t = t0 + 4 * g + r4;
; #pragma unroll
;             for (int r = 0; r < 3; ++r) { const float m = dpp_max16(fmaxf(s0, s1));
;                 const int jm = (s0 == m) ? l15 : ((s1 == m) ? l15 + 16 : 99); const int jw = dpp_min16i(jm);
;                 if (m > -INFINITY && jm == jw) { const unsigned pos = atomicAdd(&CNT[(h * 32 + jw) * 16], 1u); LIST[(size_t)h * MLIST_HEAD + moba_list_off(jw) + pos] = t * 4 + r;
;                     if (jw < 16) s0 = -INFINITY; else s1 = -INFINITY; } }
;         }
.LBB0_1906:
	s_or_b64 exec, exec, s[6:7]
	v_mov_b32_e32 v7, v15
	s_nop 1
	v_mov_b32_dpp v7, v6 quad_perm:[1,0,3,2] row_mask:0xf bank_mask:0xf
	v_max_f32_e32 v7, v7, v7
	v_max_f32_e32 v6, v6, v6
	v_max_f32_e32 v6, v6, v7
	v_mov_b32_e32 v7, v15
	s_nop 1
	v_mov_b32_dpp v7, v6 quad_perm:[2,3,0,1] row_mask:0xf bank_mask:0xf
	v_max_f32_e32 v7, v7, v7
	v_max_f32_e32 v6, v6, v7
	v_mov_b32_e32 v7, v15
	s_nop 1
	v_mov_b32_dpp v7, v6 row_half_mirror row_mask:0xf bank_mask:0xf
	v_max_f32_e32 v7, v7, v7
	v_max_f32_e32 v6, v6, v7
	v_mov_b32_e32 v7, v15
	s_nop 1
	v_mov_b32_dpp v7, v6 row_mirror row_mask:0xf bank_mask:0xf
	v_max_f32_e32 v7, v7, v7
	v_max_f32_e32 v6, v6, v7
	v_cmp_eq_f32_e64 s[4:5], v3, v6
	s_nop 1
	v_cndmask_b32_e64 v3, v20, v16, s[4:5]
	v_cmp_eq_f32_e64 s[4:5], v2, v6
	s_nop 1
	v_cndmask_b32_e64 v2, v3, v1, s[4:5]
	v_cmp_lg_f32_e64 s[4:5], s43, v6
	s_nop 0
	v_min_i32_dpp v3, v2, v2 quad_perm:[1,0,3,2] row_mask:0xf bank_mask:0xf bound_ctrl:1
	s_nop 1
	v_min_i32_dpp v3, v3, v3 quad_perm:[2,3,0,1] row_mask:0xf bank_mask:0xf bound_ctrl:1
	s_nop 1
	v_min_i32_dpp v3, v3, v3 row_half_mirror row_mask:0xf bank_mask:0xf bound_ctrl:1
	s_nop 1
	v_min_i32_dpp v3, v3, v3 row_mirror row_mask:0xf bank_mask:0xf bound_ctrl:1
	v_cmp_eq_u32_e64 s[6:7], v2, v3
	s_and_b64 s[6:7], s[4:5], s[6:7]
	s_and_saveexec_b64 s[4:5], s[6:7]
	s_cbranch_execz .LBB0_1908
	v_lshlrev_b32_e32 v3, 4, v2
	v_add_lshl_u32 v3, v3, s38, 2
	global_atomic_add v140, v3, v21, s[30:31] sc0
	v_not_b32_e32 v3, v2
	v_lshl_add_u32 v3, v3, 7, v22
	v_mul_i32_i24_e32 v2, v3, v2
	v_ashrrev_i32_e32 v3, 31, v2
	v_lshl_add_u64 v[2:3], v[2:3], 2, s[40:41]
	v_or_b32_e32 v6, 6, v23
	v_mov_b32_e32 v170, v2
	v_mov_b32_e32 v171, v3
	v_mov_b32_e32 v195, v6
	v_mov_b32_e32 v209, 1
.LBB0_1908:
	s_or_b64 exec, exec, s[4:5]
	v_cndmask_b32_e32 v2, v19, v4, vcc
	v_cndmask_b32_e64 v3, v19, v8, s[0:1]
	v_max_f32_e32 v4, v3, v3
	v_max_f32_e32 v6, v2, v2
	v_max_f32_e32 v4, v6, v4
	v_mov_b32_e32 v6, v15
	v_mov_b32_e32 v7, v15
	s_nop 0
	v_mov_b32_dpp v6, v4 quad_perm:[1,0,3,2] row_mask:0xf bank_mask:0xf
	v_max_f32_e32 v6, v6, v6
	v_max_f32_e32 v6, v4, v6
	s_nop 1
	v_mov_b32_dpp v7, v6 quad_perm:[2,3,0,1] row_mask:0xf bank_mask:0xf
	v_max_f32_e32 v7, v7, v7
	v_max_f32_e32 v6, v6, v7
	v_mov_b32_e32 v7, v15
	s_nop 1
	v_mov_b32_dpp v7, v6 row_half_mirror row_mask:0xf bank_mask:0xf
	v_max_f32_e32 v7, v7, v7
	v_max_f32_e32 v6, v6, v7
	v_mov_b32_e32 v7, v15
	s_nop 1
	v_mov_b32_dpp v7, v6 row_mirror row_mask:0xf bank_mask:0xf
	v_max_f32_e32 v7, v7, v7
	v_max_f32_e32 v7, v6, v7
	v_cmp_eq_f32_e64 s[4:5], v3, v7
	v_cmp_lg_f32_e64 s[6:7], s43, v7
	s_nop 0
	v_cndmask_b32_e64 v6, v20, v16, s[4:5]
	v_cmp_eq_f32_e64 s[4:5], v2, v7
	s_nop 1
	v_cndmask_b32_e64 v6, v6, v1, s[4:5]
	s_nop 1
	v_min_i32_dpp v8, v6, v6 quad_perm:[1,0,3,2] row_mask:0xf bank_mask:0xf bound_ctrl:1
	s_nop 1
	v_min_i32_dpp v8, v8, v8 quad_perm:[2,3,0,1] row_mask:0xf bank_mask:0xf bound_ctrl:1
	s_nop 1
	v_min_i32_dpp v8, v8, v8 row_half_mirror row_mask:0xf bank_mask:0xf bound_ctrl:1
	s_nop 1
	v_min_i32_dpp v8, v8, v8 row_mirror row_mask:0xf bank_mask:0xf bound_ctrl:1
	v_cmp_eq_u32_e64 s[8:9], v6, v8
	s_and_b64 s[8:9], s[6:7], s[8:9]
	s_and_saveexec_b64 s[6:7], s[8:9]
	s_cbranch_execz .LBB0_1910
	v_lshlrev_b32_e32 v4, 4, v6
	v_add_lshl_u32 v4, v4, s38, 2
	global_atomic_add v142, v4, v21, s[30:31] sc0
	v_not_b32_e32 v7, v6
	v_lshl_add_u32 v7, v7, 7, v22
	v_mul_i32_i24_e32 v6, v7, v6
	v_ashrrev_i32_e32 v7, 31, v6
	v_cndmask_b32_e64 v2, v2, v19, s[4:5]
	v_cndmask_b32_e64 v3, v19, v3, s[4:5]
	v_lshl_add_u64 v[6:7], v[6:7], 2, s[40:41]
	v_or_b32_e32 v4, 8, v23
	v_max_f32_e32 v8, v3, v3
	v_max_f32_e32 v24, v2, v2
	v_mov_b32_e32 v172, v6
	v_mov_b32_e32 v173, v7
	v_mov_b32_e32 v196, v4
	v_mov_b32_e32 v210, 1
	v_max_f32_e32 v4, v24, v8
.LBB0_1910:
	s_or_b64 exec, exec, s[6:7]
	v_mov_b32_e32 v6, v15
	v_max_f32_e32 v7, v4, v4
	s_nop 0
	v_mov_b32_dpp v6, v4 quad_perm:[1,0,3,2] row_mask:0xf bank_mask:0xf
	v_max_f32_e32 v6, v6, v6
	v_max_f32_e32 v6, v7, v6
	v_mov_b32_e32 v7, v15
	s_nop 1
	v_mov_b32_dpp v7, v6 quad_perm:[2,3,0,1] row_mask:0xf bank_mask:0xf
	v_max_f32_e32 v7, v7, v7
	v_max_f32_e32 v6, v6, v7
	v_mov_b32_e32 v7, v15
	s_nop 1
	v_mov_b32_dpp v7, v6 row_half_mirror row_mask:0xf bank_mask:0xf
	v_max_f32_e32 v7, v7, v7
	v_max_f32_e32 v6, v6, v7
	v_mov_b32_e32 v7, v15
	s_nop 1
	v_mov_b32_dpp v7, v6 row_mirror row_mask:0xf bank_mask:0xf
	v_max_f32_e32 v7, v7, v7
	v_max_f32_e32 v7, v6, v7
	v_cmp_eq_f32_e64 s[4:5], v3, v7
	v_cmp_lg_f32_e64 s[6:7], s43, v7
	s_nop 0
	v_cndmask_b32_e64 v6, v20, v16, s[4:5]
	v_cmp_eq_f32_e64 s[4:5], v2, v7
	s_nop 1
	v_cndmask_b32_e64 v6, v6, v1, s[4:5]
	s_nop 1
	v_min_i32_dpp v8, v6, v6 quad_perm:[1,0,3,2] row_mask:0xf bank_mask:0xf bound_ctrl:1
	s_nop 1
	v_min_i32_dpp v8, v8, v8 quad_perm:[2,3,0,1] row_mask:0xf bank_mask:0xf bound_ctrl:1
	s_nop 1
	v_min_i32_dpp v8, v8, v8 row_half_mirror row_mask:0xf bank_mask:0xf bound_ctrl:1
	s_nop 1
	v_min_i32_dpp v8, v8, v8 row_mirror row_mask:0xf bank_mask:0xf bound_ctrl:1
	v_cmp_eq_u32_e64 s[8:9], v6, v8
	s_and_b64 s[8:9], s[6:7], s[8:9]
	s_and_saveexec_b64 s[6:7], s[8:9]
	s_cbranch_execz .LBB0_1912
	v_lshlrev_b32_e32 v4, 4, v6
	v_add_lshl_u32 v4, v4, s38, 2
	global_atomic_add v144, v4, v21, s[30:31] sc0
	v_not_b32_e32 v7, v6
	v_lshl_add_u32 v7, v7, 7, v22
	v_mul_i32_i24_e32 v6, v7, v6
	v_ashrrev_i32_e32 v7, 31, v6
	v_cndmask_b32_e64 v2, v2, v19, s[4:5]
	v_cndmask_b32_e64 v3, v19, v3, s[4:5]
	v_lshl_add_u64 v[6:7], v[6:7], 2, s[40:41]
	v_or_b32_e32 v4, 9, v23
	v_max_f32_e32 v8, v3, v3
	v_max_f32_e32 v24, v2, v2
	v_mov_b32_e32 v174, v6
	v_mov_b32_e32 v175, v7
	v_mov_b32_e32 v197, v4
	v_mov_b32_e32 v211, 1
	v_max_f32_e32 v4, v24, v8
; __device__ __forceinline__ void p4_moba_gate(Frame& F) {
;     ...
;         for (int r4 = 0; r4 < 4; ++r4) {
;             float s0 = l15 < blk ? acc[0][r4] : -INFINITY, s1 = l15 + 16 < blk ? acc[1][r4] : -INFINITY;
;             const int t = t0 + 4 * g + r4;
; #pragma unroll
;             for (int r = 0; r < 3; ++r) { const float m = dpp_max16(fmaxf(s0, s1));
;                 const int jm = (s0 == m) ? l15 : ((s1 == m) ? l15 + 16 : 99); const int jw = dpp_min16i(jm);
;                 if (m > -INFINITY && jm == jw) { const unsigned pos = atomicAdd(&CNT[(h * 32 + jw) * 16], 1u); LIST[(size_t)h * MLIST_HEAD + moba_list_off(jw) + pos] = t * 4 + r;
;                     if (jw < 16) s0 = -INFINITY; else s1 = -INFINITY; } }
;         }
.LBB0_1912:
	s_or_b64 exec, exec, s[6:7]
	v_mov_b32_e32 v6, v15
	s_nop 1
	v_mov_b32_dpp v6, v4 quad_perm:[1,0,3,2] row_mask:0xf bank_mask:0xf
	v_max_f32_e32 v6, v6, v6
	v_max_f32_e32 v4, v4, v4
	v_max_f32_e32 v4, v4, v6
	v_mov_b32_e32 v6, v15
	s_nop 1
	v_mov_b32_dpp v6, v4 quad_perm:[2,3,0,1] row_mask:0xf bank_mask:0xf
	v_max_f32_e32 v6, v6, v6
	v_max_f32_e32 v4, v4, v6
	v_mov_b32_e32 v6, v15
	s_nop 1
	v_mov_b32_dpp v6, v4 row_half_mirror row_mask:0xf bank_mask:0xf
	v_max_f32_e32 v6, v6, v6
	v_max_f32_e32 v4, v4, v6
	v_mov_b32_e32 v6, v15
	s_nop 1
	v_mov_b32_dpp v6, v4 row_mirror row_mask:0xf bank_mask:0xf
	v_max_f32_e32 v6, v6, v6
	v_max_f32_e32 v4, v4, v6
	v_cmp_eq_f32_e64 s[4:5], v3, v4
	s_nop 1
	v_cndmask_b32_e64 v3, v20, v16, s[4:5]
	v_cmp_eq_f32_e64 s[4:5], v2, v4
	s_nop 1
	v_cndmask_b32_e64 v2, v3, v1, s[4:5]
	v_cmp_lg_f32_e64 s[4:5], s43, v4
	s_nop 0
	v_min_i32_dpp v3, v2, v2 quad_perm:[1,0,3,2] row_mask:0xf bank_mask:0xf bound_ctrl:1
	s_nop 1
	v_min_i32_dpp v3, v3, v3 quad_perm:[2,3,0,1] row_mask:0xf bank_mask:0xf bound_ctrl:1
	s_nop 1
	v_min_i32_dpp v3, v3, v3 row_half_mirror row_mask:0xf bank_mask:0xf bound_ctrl:1
	s_nop 1
	v_min_i32_dpp v3, v3, v3 row_mirror row_mask:0xf bank_mask:0xf bound_ctrl:1
	v_cmp_eq_u32_e64 s[6:7], v2, v3
	s_and_b64 s[6:7], s[4:5], s[6:7]
	s_and_saveexec_b64 s[4:5], s[6:7]
	s_cbranch_execz .LBB0_1914
	v_lshlrev_b32_e32 v3, 4, v2
	v_add_lshl_u32 v3, v3, s38, 2
	global_atomic_add v146, v3, v21, s[30:31] sc0
	v_not_b32_e32 v3, v2
	v_lshl_add_u32 v3, v3, 7, v22
	v_mul_i32_i24_e32 v2, v3, v2
	v_ashrrev_i32_e32 v3, 31, v2
	v_lshl_add_u64 v[2:3], v[2:3], 2, s[40:41]
	v_or_b32_e32 v4, 10, v23
	v_mov_b32_e32 v176, v2
	v_mov_b32_e32 v177, v3
	v_mov_b32_e32 v198, v4
	v_mov_b32_e32 v212, 1
.LBB0_1914:
	s_or_b64 exec, exec, s[4:5]
	v_cndmask_b32_e32 v2, v19, v5, vcc
	v_cndmask_b32_e64 v3, v19, v9, s[0:1]
	v_max_f32_e32 v4, v3, v3
	v_max_f32_e32 v5, v2, v2
	v_max_f32_e32 v4, v5, v4
	v_mov_b32_e32 v5, v15
	v_mov_b32_e32 v6, v15
	s_nop 0
	v_mov_b32_dpp v5, v4 quad_perm:[1,0,3,2] row_mask:0xf bank_mask:0xf
	v_max_f32_e32 v5, v5, v5
	v_max_f32_e32 v5, v4, v5
	s_nop 1
	v_mov_b32_dpp v6, v5 quad_perm:[2,3,0,1] row_mask:0xf bank_mask:0xf
	v_max_f32_e32 v6, v6, v6
	v_max_f32_e32 v5, v5, v6
	v_mov_b32_e32 v6, v15
	s_nop 1
	v_mov_b32_dpp v6, v5 row_half_mirror row_mask:0xf bank_mask:0xf
	v_max_f32_e32 v6, v6, v6
	v_max_f32_e32 v5, v5, v6
	v_mov_b32_e32 v6, v15
	s_nop 1
	v_mov_b32_dpp v6, v5 row_mirror row_mask:0xf bank_mask:0xf
	v_max_f32_e32 v6, v6, v6
	v_max_f32_e32 v6, v5, v6
	v_cmp_eq_f32_e32 vcc, v3, v6
	v_cmp_lg_f32_e64 s[0:1], s43, v6
	s_nop 0
	v_cndmask_b32_e32 v5, v20, v16, vcc
	v_cmp_eq_f32_e32 vcc, v2, v6
	s_nop 1
	v_cndmask_b32_e32 v5, v5, v1, vcc
	s_nop 1
	v_min_i32_dpp v7, v5, v5 quad_perm:[1,0,3,2] row_mask:0xf bank_mask:0xf bound_ctrl:1
	s_nop 1
	v_min_i32_dpp v7, v7, v7 quad_perm:[2,3,0,1] row_mask:0xf bank_mask:0xf bound_ctrl:1
	s_nop 1
	v_min_i32_dpp v7, v7, v7 row_half_mirror row_mask:0xf bank_mask:0xf bound_ctrl:1
	s_nop 1
	v_min_i32_dpp v7, v7, v7 row_mirror row_mask:0xf bank_mask:0xf bound_ctrl:1
	v_cmp_eq_u32_e64 s[4:5], v5, v7
	s_and_b64 s[4:5], s[0:1], s[4:5]
	s_and_saveexec_b64 s[0:1], s[4:5]
	s_cbranch_execz .LBB0_1916
	v_lshlrev_b32_e32 v4, 4, v5
	v_add_lshl_u32 v4, v4, s38, 2
	global_atomic_add v148, v4, v21, s[30:31] sc0
	v_not_b32_e32 v4, v5
	v_lshl_add_u32 v4, v4, 7, v22
	v_mul_i32_i24_e32 v4, v4, v5
	v_ashrrev_i32_e32 v5, 31, v4
	v_cndmask_b32_e32 v2, v2, v19, vcc
	v_cndmask_b32_e32 v3, v19, v3, vcc
	v_lshl_add_u64 v[4:5], v[4:5], 2, s[40:41]
	v_or_b32_e32 v6, 12, v23
	v_max_f32_e32 v7, v3, v3
	v_max_f32_e32 v8, v2, v2
	v_mov_b32_e32 v178, v4
	v_mov_b32_e32 v179, v5
	v_mov_b32_e32 v199, v6
	v_mov_b32_e32 v213, 1
	v_max_f32_e32 v4, v8, v7
; __device__ __forceinline__ void p4_moba_gate(Frame& F) {
;     ...
;         for (int r4 = 0; r4 < 4; ++r4) {
;             float s0 = l15 < blk ? acc[0][r4] : -INFINITY, s1 = l15 + 16 < blk ? acc[1][r4] : -INFINITY;
;             const int t = t0 + 4 * g + r4;
; #pragma unroll
;             for (int r = 0; r < 3; ++r) { const float m = dpp_max16(fmaxf(s0, s1));
;                 const int jm = (s0 == m) ? l15 : ((s1 == m) ? l15 + 16 : 99); const int jw = dpp_min16i(jm);
;                 if (m > -INFINITY && jm == jw) { const unsigned pos = atomicAdd(&CNT[(h * 32 + jw) * 16], 1u); LIST[(size_t)h * MLIST_HEAD + moba_list_off(jw) + pos] = t * 4 + r;
;                     if (jw < 16) s0 = -INFINITY; else s1 = -INFINITY; } }
;         }
.LBB0_1916:
	s_or_b64 exec, exec, s[0:1]
	v_mov_b32_e32 v5, v15
	v_max_f32_e32 v6, v4, v4
	s_nop 0
	v_mov_b32_dpp v5, v4 quad_perm:[1,0,3,2] row_mask:0xf bank_mask:0xf
	v_max_f32_e32 v5, v5, v5
	v_max_f32_e32 v5, v6, v5
	v_mov_b32_e32 v6, v15
	s_nop 1
	v_mov_b32_dpp v6, v5 quad_perm:[2,3,0,1] row_mask:0xf bank_mask:0xf
	v_max_f32_e32 v6, v6, v6
	v_max_f32_e32 v5, v5, v6
	v_mov_b32_e32 v6, v15
	s_nop 1
	v_mov_b32_dpp v6, v5 row_half_mirror row_mask:0xf bank_mask:0xf
	v_max_f32_e32 v6, v6, v6
	v_max_f32_e32 v5, v5, v6
	v_mov_b32_e32 v6, v15
	s_nop 1
	v_mov_b32_dpp v6, v5 row_mirror row_mask:0xf bank_mask:0xf
	v_max_f32_e32 v6, v6, v6
	v_max_f32_e32 v6, v5, v6
	v_cmp_eq_f32_e32 vcc, v3, v6
	v_cmp_lg_f32_e64 s[0:1], s43, v6
	s_nop 0
	v_cndmask_b32_e32 v5, v20, v16, vcc
	v_cmp_eq_f32_e32 vcc, v2, v6
	s_nop 1
	v_cndmask_b32_e32 v5, v5, v1, vcc
	s_nop 1
	v_min_i32_dpp v7, v5, v5 quad_perm:[1,0,3,2] row_mask:0xf bank_mask:0xf bound_ctrl:1
	s_nop 1
	v_min_i32_dpp v7, v7, v7 quad_perm:[2,3,0,1] row_mask:0xf bank_mask:0xf bound_ctrl:1
	s_nop 1
	v_min_i32_dpp v7, v7, v7 row_half_mirror row_mask:0xf bank_mask:0xf bound_ctrl:1
	s_nop 1
	v_min_i32_dpp v7, v7, v7 row_mirror row_mask:0xf bank_mask:0xf bound_ctrl:1
	v_cmp_eq_u32_e64 s[4:5], v5, v7
	s_and_b64 s[4:5], s[0:1], s[4:5]
	s_and_saveexec_b64 s[0:1], s[4:5]
	s_cbranch_execz .LBB0_1918
	v_lshlrev_b32_e32 v4, 4, v5
	v_add_lshl_u32 v4, v4, s38, 2
	global_atomic_add v150, v4, v21, s[30:31] sc0
	v_not_b32_e32 v4, v5
	v_lshl_add_u32 v4, v4, 7, v22
	v_mul_i32_i24_e32 v4, v4, v5
	v_ashrrev_i32_e32 v5, 31, v4
	v_cndmask_b32_e32 v2, v2, v19, vcc
	v_cndmask_b32_e32 v3, v19, v3, vcc
	v_lshl_add_u64 v[4:5], v[4:5], 2, s[40:41]
	v_or_b32_e32 v6, 13, v23
	v_max_f32_e32 v7, v3, v3
	v_max_f32_e32 v8, v2, v2
	v_mov_b32_e32 v180, v4
	v_mov_b32_e32 v181, v5
	v_mov_b32_e32 v200, v6
	v_mov_b32_e32 v214, 1
	v_max_f32_e32 v4, v8, v7
.LBB0_1918:
	s_or_b64 exec, exec, s[0:1]
	v_mov_b32_e32 v5, v15
	s_nop 1
	v_mov_b32_dpp v5, v4 quad_perm:[1,0,3,2] row_mask:0xf bank_mask:0xf
	v_max_f32_e32 v5, v5, v5
	v_max_f32_e32 v4, v4, v4
	v_max_f32_e32 v4, v4, v5
	v_mov_b32_e32 v5, v15
	s_nop 1
	v_mov_b32_dpp v5, v4 quad_perm:[2,3,0,1] row_mask:0xf bank_mask:0xf
	v_max_f32_e32 v5, v5, v5
	v_max_f32_e32 v4, v4, v5
	v_mov_b32_e32 v5, v15
	s_nop 1
	v_mov_b32_dpp v5, v4 row_half_mirror row_mask:0xf bank_mask:0xf
	v_max_f32_e32 v5, v5, v5
	v_max_f32_e32 v4, v4, v5
	v_mov_b32_e32 v5, v15
	s_nop 1
	v_mov_b32_dpp v5, v4 row_mirror row_mask:0xf bank_mask:0xf
	v_max_f32_e32 v5, v5, v5
	v_max_f32_e32 v4, v4, v5
	v_cmp_eq_f32_e32 vcc, v3, v4
	s_nop 1
	v_cndmask_b32_e32 v3, v20, v16, vcc
	v_cmp_eq_f32_e32 vcc, v2, v4
	s_nop 1
	v_cndmask_b32_e32 v2, v3, v1, vcc
	v_cmp_lg_f32_e32 vcc, s43, v4
	s_nop 0
	v_min_i32_dpp v3, v2, v2 quad_perm:[1,0,3,2] row_mask:0xf bank_mask:0xf bound_ctrl:1
	s_nop 1
	v_min_i32_dpp v3, v3, v3 quad_perm:[2,3,0,1] row_mask:0xf bank_mask:0xf bound_ctrl:1
	s_nop 1
	v_min_i32_dpp v3, v3, v3 row_half_mirror row_mask:0xf bank_mask:0xf bound_ctrl:1
	s_nop 1
	v_min_i32_dpp v3, v3, v3 row_mirror row_mask:0xf bank_mask:0xf bound_ctrl:1
	v_cmp_eq_u32_e64 s[0:1], v2, v3
	s_and_b64 s[4:5], vcc, s[0:1]
	s_and_saveexec_b64 s[0:1], s[4:5]
	s_cbranch_execz .LBB0_1895
	v_lshlrev_b32_e32 v3, 4, v2
	v_add_lshl_u32 v3, v3, s38, 2
	global_atomic_add v152, v3, v21, s[30:31] sc0
	v_not_b32_e32 v3, v2
	v_lshl_add_u32 v3, v3, 7, v22
	v_mul_i32_i24_e32 v2, v3, v2
	v_ashrrev_i32_e32 v3, 31, v2
	v_lshl_add_u64 v[2:3], v[2:3], 2, s[40:41]
	v_or_b32_e32 v4, 14, v23
	v_mov_b32_e32 v182, v2
	v_mov_b32_e32 v183, v3
	v_mov_b32_e32 v201, v4
	v_mov_b32_e32 v215, 1
	s_branch .LBB0_1895

; #define P12_VISSUE(c_, i_, q_, D_X) do { _Pragma("unroll") for (int b = 0; b < 8; ++b) { const int idx = ((q_) * 8 + b) * 4 + eg; const unsigned ro = (unsigned)(c_) * 16384u + (unsigned)EL[(i_) * 128 + idx]; \
;           const v3u_ ld_ = *(const v3u_*)(V8 + (size_t)(ro * 192u + 12u * (unsigned)cl)); if (b & 1) D_X[b >> 1].hi = ld_; else D_X[b >> 1].lo = ld_; } } while (0)
; __device__ __forceinline__ void p12_peer(Frame& F) {
;     ...
;       v6u_ dA[4], dB[4];
;       P12_VISSUE(0, 0, 0, dA);
; _Pragma("nounroll")
;       for (int c = 0; c < 16; ++c) {
;           int lo_ = 16 * cl + 4 * eg; asm volatile("" : "+v"(lo_));
; _Pragma("nounroll")
;           for (int i = 0; i < 4; ++i) { const int t = F.gw + i * F.NGW;
;               f32x2 acc2[8];
; #pragma unroll
;               for (int m = 0; m < 8; ++m) acc2[m] = (f32x2){0.f, 0.f};
;               const v2u hb = *(const v2u*)(HN + ((size_t)t * D_ + (size_t)(unsigned)(256 * c + lo_)));
;               P12_VISSUE(c, i, 1, dB); asm volatile("" ::: "memory"); P12_VCOMP(i, 0, dA);
;               P12_VISSUE(c, i, 2, dA); asm volatile("" ::: "memory"); P12_VCOMP(i, 1, dB);
;               P12_VISSUE(c, i, 3, dB); asm volatile("" ::: "memory"); P12_VCOMP(i, 2, dA);
;               { const int in_ = i + 1 < 4 ? i + 1 : 0, cn_ = i + 1 < 4 ? c : (c + 1 < 16 ? c + 1 : 15); P12_VISSUE(cn_, in_, 0, dA); } asm volatile("" ::: "memory"); P12_VCOMP(i, 3, dB);
.LBB0_3403:
	v_add_u32_e32 v152, s28, v175
	ds_read_u16 v2, v152
	ds_read_u16 v3, v152 offset:8
	ds_read_u16 v4, v152 offset:16
	ds_read_u16 v5, v152 offset:24
	ds_read_u16 v6, v152 offset:32
	ds_read_u16 v7, v152 offset:40
	ds_read_u16 v8, v152 offset:48
	ds_read_u16 v9, v152 offset:56
	s_ashr_i32 s13, s12, 31
	s_lshl_b64 s[14:15], s[12:13], 13
	v_lshl_add_u64 v[0:1], v[164:165], 0, s[14:15]
	s_cmpk_eq_i32 s28, 0x300
	global_load_dwordx2 v[158:159], v[0:1], off
	s_cselect_b32 s30, 0, s23
	s_waitcnt lgkmcnt(7)
	v_add_u32_e32 v0, s21, v2
	v_lshl_add_u32 v179, s30, 1, v161
	s_waitcnt lgkmcnt(6)
	v_add_u32_e32 v2, s21, v3
	s_waitcnt lgkmcnt(5)
	v_add_u32_e32 v4, s21, v4
	s_waitcnt lgkmcnt(4)
	v_add_u32_e32 v10, s21, v5
	s_waitcnt lgkmcnt(3)
	v_add_u32_e32 v11, s21, v6
	s_waitcnt lgkmcnt(2)
	v_add_u32_e32 v12, s21, v7
	s_waitcnt lgkmcnt(1)
	v_add_u32_e32 v13, s21, v8
	s_waitcnt lgkmcnt(0)
	v_add_u32_e32 v14, s21, v9
	v_mad_u32_u24 v0, v0, s16, v160
	v_mad_u32_u24 v2, v2, s16, v160
	v_mad_u32_u24 v4, v4, s16, v160
	v_mad_u32_u24 v6, v10, s16, v160
	v_mad_u32_u24 v8, v11, s16, v160
	v_mad_u32_u24 v10, v12, s16, v160
	v_mad_u32_u24 v12, v13, s16, v160
	v_mad_u32_u24 v14, v14, s16, v160
	global_load_dwordx3 v[154:156], v0, s[2:3]
	global_load_dwordx3 v[220:222], v2, s[2:3]
	global_load_dwordx3 v[180:182], v4, s[2:3]
	global_load_dwordx3 v[224:226], v6, s[2:3]
	global_load_dwordx3 v[186:188], v8, s[2:3]
	global_load_dwordx3 v[228:230], v10, s[2:3]
	global_load_dwordx3 v[192:194], v12, s[2:3]
	global_load_dwordx3 v[232:234], v14, s[2:3]
	ds_read2_b32 v[166:167], v177 offset1:4
	ds_read2_b32 v[168:169], v177 offset0:8 offset1:12
	s_waitcnt vmcnt(10)
	ds_read2_b32 v[184:185], v177 offset0:16 offset1:20
	s_waitcnt vmcnt(9)
	ds_read2_b32 v[190:191], v177 offset0:24 offset1:28
	v_cvt_scalef32_pk32_f32_fp6 v[96:127], v[134:139], 1.0
	v_cvt_scalef32_pk32_f32_fp6 v[64:95], v[128:133], 1.0
	ds_read_u16 v129, v152 offset:64
	ds_read_u16 v131, v152 offset:72
	ds_read_u16 v132, v152 offset:80
	ds_read_u16 v133, v152 offset:88
	ds_read_u16 v134, v152 offset:96
	ds_read_u16 v135, v152 offset:104
	ds_read_u16 v136, v152 offset:112
	ds_read_u16 v137, v152 offset:120
	s_waitcnt lgkmcnt(11)
	v_pk_fma_f32 v[96:97], v[96:97], v[166:167], 0 op_sel_hi:[1,0,0]
	v_pk_fma_f32 v[98:99], v[98:99], v[166:167], 0 op_sel_hi:[1,0,0]
	v_pk_fma_f32 v[100:101], v[100:101], v[166:167], 0 op_sel_hi:[1,0,0]
	v_pk_fma_f32 v[102:103], v[102:103], v[166:167], 0 op_sel_hi:[1,0,0]
	v_pk_fma_f32 v[104:105], v[104:105], v[166:167], 0 op_sel_hi:[1,0,0]
	v_pk_fma_f32 v[106:107], v[106:107], v[166:167], 0 op_sel_hi:[1,0,0]
	v_pk_fma_f32 v[108:109], v[108:109], v[166:167], 0 op_sel_hi:[1,0,0]
	v_pk_fma_f32 v[110:111], v[110:111], v[166:167], 0 op_sel_hi:[1,0,0]
	v_mov_b32_e32 v128, v167
	s_waitcnt lgkmcnt(7)
	v_pk_fma_f32 v[96:97], v[112:113], v[128:129], v[96:97] op_sel_hi:[1,0,1]
	v_pk_fma_f32 v[98:99], v[114:115], v[128:129], v[98:99] op_sel_hi:[1,0,1]
	v_pk_fma_f32 v[100:101], v[116:117], v[128:129], v[100:101] op_sel_hi:[1,0,1]
	v_pk_fma_f32 v[102:103], v[118:119], v[128:129], v[102:103] op_sel_hi:[1,0,1]
	v_pk_fma_f32 v[104:105], v[120:121], v[128:129], v[104:105] op_sel_hi:[1,0,1]
	v_pk_fma_f32 v[106:107], v[122:123], v[128:129], v[106:107] op_sel_hi:[1,0,1]
	v_pk_fma_f32 v[108:109], v[124:125], v[128:129], v[108:109] op_sel_hi:[1,0,1]
	v_pk_fma_f32 v[110:111], v[126:127], v[128:129], v[110:111] op_sel_hi:[1,0,1]
	v_add_u32_e32 v112, s21, v129
	v_mov_b32_e32 v130, v169
	s_waitcnt lgkmcnt(6)
	v_add_u32_e32 v113, s21, v131
	s_waitcnt lgkmcnt(5)
	v_add_u32_e32 v114, s21, v132
	s_waitcnt lgkmcnt(4)
	v_add_u32_e32 v115, s21, v133
	s_waitcnt lgkmcnt(3)
	v_add_u32_e32 v116, s21, v134
	s_waitcnt lgkmcnt(2)
	v_add_u32_e32 v117, s21, v135
	s_waitcnt lgkmcnt(1)
	v_add_u32_e32 v118, s21, v136
	s_waitcnt lgkmcnt(0)
	v_add_u32_e32 v119, s21, v137
	v_pk_fma_f32 v[64:65], v[64:65], v[168:169], v[96:97] op_sel_hi:[1,0,1]
	v_pk_fma_f32 v[66:67], v[66:67], v[168:169], v[98:99] op_sel_hi:[1,0,1]
	v_pk_fma_f32 v[68:69], v[68:69], v[168:169], v[100:101] op_sel_hi:[1,0,1]
	v_pk_fma_f32 v[70:71], v[70:71], v[168:169], v[102:103] op_sel_hi:[1,0,1]
	v_pk_fma_f32 v[72:73], v[72:73], v[168:169], v[104:105] op_sel_hi:[1,0,1]
	v_pk_fma_f32 v[74:75], v[74:75], v[168:169], v[106:107] op_sel_hi:[1,0,1]
	v_pk_fma_f32 v[76:77], v[76:77], v[168:169], v[108:109] op_sel_hi:[1,0,1]
	v_pk_fma_f32 v[78:79], v[78:79], v[168:169], v[110:111] op_sel_hi:[1,0,1]
	v_mad_u32_u24 v96, v112, s16, v160
	v_cvt_scalef32_pk32_f32_fp6 v[32:63], v[140:145], 1.0
	v_mad_u32_u24 v98, v113, s16, v160
	v_mad_u32_u24 v100, v114, s16, v160
	v_mad_u32_u24 v102, v115, s16, v160
	v_mad_u32_u24 v104, v116, s16, v160
	v_mad_u32_u24 v106, v117, s16, v160
	v_mad_u32_u24 v108, v118, s16, v160
	v_mad_u32_u24 v110, v119, s16, v160
	v_pk_fma_f32 v[64:65], v[80:81], v[130:131], v[64:65] op_sel_hi:[1,0,1]
	v_pk_fma_f32 v[66:67], v[82:83], v[130:131], v[66:67] op_sel_hi:[1,0,1]
	v_pk_fma_f32 v[68:69], v[84:85], v[130:131], v[68:69] op_sel_hi:[1,0,1]
	v_pk_fma_f32 v[70:71], v[86:87], v[130:131], v[70:71] op_sel_hi:[1,0,1]
	v_pk_fma_f32 v[72:73], v[88:89], v[130:131], v[72:73] op_sel_hi:[1,0,1]
	v_pk_fma_f32 v[74:75], v[90:91], v[130:131], v[74:75] op_sel_hi:[1,0,1]
	v_pk_fma_f32 v[76:77], v[92:93], v[130:131], v[76:77] op_sel_hi:[1,0,1]
	v_pk_fma_f32 v[78:79], v[94:95], v[130:131], v[78:79] op_sel_hi:[1,0,1]
	global_load_dwordx3 v[198:200], v96, s[2:3]
	global_load_dwordx3 v[128:130], v98, s[2:3]
	global_load_dwordx3 v[204:206], v100, s[2:3]
	global_load_dwordx3 v[132:134], v102, s[2:3]
	global_load_dwordx3 v[210:212], v104, s[2:3]
	global_load_dwordx3 v[136:138], v106, s[2:3]
	global_load_dwordx3 v[216:218], v108, s[2:3]
	global_load_dwordx3 v[140:142], v110, s[2:3]
	v_mov_b32_e32 v144, v185
	v_pk_fma_f32 v[32:33], v[32:33], v[184:185], v[64:65] op_sel_hi:[1,0,1]
	v_pk_fma_f32 v[34:35], v[34:35], v[184:185], v[66:67] op_sel_hi:[1,0,1]
	v_pk_fma_f32 v[36:37], v[36:37], v[184:185], v[68:69] op_sel_hi:[1,0,1]
	v_pk_fma_f32 v[38:39], v[38:39], v[184:185], v[70:71] op_sel_hi:[1,0,1]
	v_pk_fma_f32 v[40:41], v[40:41], v[184:185], v[72:73] op_sel_hi:[1,0,1]
	v_pk_fma_f32 v[42:43], v[42:43], v[184:185], v[74:75] op_sel_hi:[1,0,1]
	v_pk_fma_f32 v[44:45], v[44:45], v[184:185], v[76:77] op_sel_hi:[1,0,1]
	v_pk_fma_f32 v[46:47], v[46:47], v[184:185], v[78:79] op_sel_hi:[1,0,1]
	v_cvt_scalef32_pk32_f32_fp6 v[0:31], v[146:151], 1.0
	v_pk_fma_f32 v[32:33], v[48:49], v[144:145], v[32:33] op_sel_hi:[1,0,1]
	v_pk_fma_f32 v[34:35], v[50:51], v[144:145], v[34:35] op_sel_hi:[1,0,1]
	v_pk_fma_f32 v[36:37], v[52:53], v[144:145], v[36:37] op_sel_hi:[1,0,1]
	v_pk_fma_f32 v[38:39], v[54:55], v[144:145], v[38:39] op_sel_hi:[1,0,1]
	v_pk_fma_f32 v[40:41], v[56:57], v[144:145], v[40:41] op_sel_hi:[1,0,1]
	v_pk_fma_f32 v[42:43], v[58:59], v[144:145], v[42:43] op_sel_hi:[1,0,1]
	v_pk_fma_f32 v[44:45], v[60:61], v[144:145], v[44:45] op_sel_hi:[1,0,1]
	v_pk_fma_f32 v[46:47], v[62:63], v[144:145], v[46:47] op_sel_hi:[1,0,1]
	s_waitcnt vmcnt(16)
; #define P12_VISSUE(c_, i_, q_, D_X) do { _Pragma("unroll") for (int b = 0; b < 8; ++b) { const int idx = ((q_) * 8 + b) * 4 + eg; const unsigned ro = (unsigned)(c_) * 16384u + (unsigned)EL[(i_) * 128 + idx]; \
;           const v3u_ ld_ = *(const v3u_*)(V8 + (size_t)(ro * 192u + 12u * (unsigned)cl)); if (b & 1) D_X[b >> 1].hi = ld_; else D_X[b >> 1].lo = ld_; } } while (0)
; __device__ __forceinline__ void p12_peer(Frame& F) {
;     ...
;       v6u_ dA[4], dB[4];
;       P12_VISSUE(0, 0, 0, dA);
; _Pragma("nounroll")
;       for (int c = 0; c < 16; ++c) {
;           int lo_ = 16 * cl + 4 * eg; asm volatile("" : "+v"(lo_));
; _Pragma("nounroll")
;           for (int i = 0; i < 4; ++i) { const int t = F.gw + i * F.NGW;
;               f32x2 acc2[8];
; #pragma unroll
;               for (int m = 0; m < 8; ++m) acc2[m] = (f32x2){0.f, 0.f};
;               const v2u hb = *(const v2u*)(HN + ((size_t)t * D_ + (size_t)(unsigned)(256 * c + lo_)));
;               P12_VISSUE(c, i, 1, dB); asm volatile("" ::: "memory"); P12_VCOMP(i, 0, dA);
;               P12_VISSUE(c, i, 2, dA); asm volatile("" ::: "memory"); P12_VCOMP(i, 1, dB);
;               P12_VISSUE(c, i, 3, dB); asm volatile("" ::: "memory"); P12_VCOMP(i, 2, dA);
;               { const int in_ = i + 1 < 4 ? i + 1 : 0, cn_ = i + 1 < 4 ? c : (c + 1 < 16 ? c + 1 : 15); P12_VISSUE(cn_, in_, 0, dA); } asm volatile("" ::: "memory"); P12_VCOMP(i, 3, dB);
	v_lshlrev_b32_e32 v167, 16, v159
	v_lshlrev_b32_e32 v166, 16, v158
	v_and_b32_e32 v169, 0xffff0000, v159
	v_and_b32_e32 v168, 0xffff0000, v158
	s_waitcnt vmcnt(14)
	v_mov_b32_e32 v157, v220
	v_mov_b32_e32 v158, v221
	v_mov_b32_e32 v159, v222
	v_mov_b32_e32 v146, v191
	v_pk_fma_f32 v[0:1], v[0:1], v[190:191], v[32:33] op_sel_hi:[1,0,1]
	v_pk_fma_f32 v[2:3], v[2:3], v[190:191], v[34:35] op_sel_hi:[1,0,1]
	v_pk_fma_f32 v[4:5], v[4:5], v[190:191], v[36:37] op_sel_hi:[1,0,1]
	v_pk_fma_f32 v[6:7], v[6:7], v[190:191], v[38:39] op_sel_hi:[1,0,1]
	v_pk_fma_f32 v[8:9], v[8:9], v[190:191], v[40:41] op_sel_hi:[1,0,1]
	v_pk_fma_f32 v[10:11], v[10:11], v[190:191], v[42:43] op_sel_hi:[1,0,1]
	v_pk_fma_f32 v[12:13], v[12:13], v[190:191], v[44:45] op_sel_hi:[1,0,1]
	v_pk_fma_f32 v[14:15], v[14:15], v[190:191], v[46:47] op_sel_hi:[1,0,1]
	s_waitcnt vmcnt(12)
	v_mov_b32_e32 v183, v224
	v_mov_b32_e32 v184, v225
	v_mov_b32_e32 v185, v226
	s_waitcnt vmcnt(10)
	v_mov_b32_e32 v189, v228
	v_mov_b32_e32 v190, v229
	v_mov_b32_e32 v191, v230
	s_waitcnt vmcnt(8)
	v_mov_b32_e32 v195, v232
	v_mov_b32_e32 v196, v233
	v_mov_b32_e32 v197, v234
	ds_read2_b32 v[220:221], v177 offset0:32 offset1:36
	ds_read2_b32 v[222:223], v177 offset0:40 offset1:44
	ds_read2_b32 v[242:243], v177 offset0:48 offset1:52
	ds_read2_b32 v[244:245], v177 offset0:56 offset1:60
	v_cvt_scalef32_pk32_f32_fp6 v[96:127], v[154:159], 1.0
	ds_read_u16 v131, v152 offset:128
	ds_read_u16 v135, v152 offset:136
	ds_read_u16 v139, v152 offset:144
	ds_read_u16 v143, v152 offset:152
	ds_read_u16 v153, v152 offset:160
	ds_read_u16 v154, v152 offset:168
	ds_read_u16 v155, v152 offset:176
	ds_read_u16 v152, v152 offset:184
	v_pk_fma_f32 v[144:145], v[16:17], v[146:147], v[0:1] op_sel_hi:[1,0,1]
	v_pk_fma_f32 v[148:149], v[18:19], v[146:147], v[2:3] op_sel_hi:[1,0,1]
	v_pk_fma_f32 v[150:151], v[20:21], v[146:147], v[4:5] op_sel_hi:[1,0,1]
	v_pk_fma_f32 v[202:203], v[22:23], v[146:147], v[6:7] op_sel_hi:[1,0,1]
	v_pk_fma_f32 v[208:209], v[24:25], v[146:147], v[8:9] op_sel_hi:[1,0,1]
	v_pk_fma_f32 v[214:215], v[26:27], v[146:147], v[10:11] op_sel_hi:[1,0,1]
	v_pk_fma_f32 v[236:237], v[28:29], v[146:147], v[12:13] op_sel_hi:[1,0,1]
	v_pk_fma_f32 v[146:147], v[30:31], v[146:147], v[14:15] op_sel_hi:[1,0,1]
	s_waitcnt lgkmcnt(11)
	v_pk_fma_f32 v[96:97], v[96:97], v[220:221], v[144:145] op_sel_hi:[1,0,1]
	v_mov_b32_e32 v144, v221
	v_cvt_scalef32_pk32_f32_fp6 v[64:95], v[180:185], 1.0
	v_pk_fma_f32 v[98:99], v[98:99], v[220:221], v[148:149] op_sel_hi:[1,0,1]
	v_pk_fma_f32 v[100:101], v[100:101], v[220:221], v[150:151] op_sel_hi:[1,0,1]
	v_pk_fma_f32 v[102:103], v[102:103], v[220:221], v[202:203] op_sel_hi:[1,0,1]
	v_pk_fma_f32 v[104:105], v[104:105], v[220:221], v[208:209] op_sel_hi:[1,0,1]
	v_pk_fma_f32 v[106:107], v[106:107], v[220:221], v[214:215] op_sel_hi:[1,0,1]
	v_pk_fma_f32 v[108:109], v[108:109], v[220:221], v[236:237] op_sel_hi:[1,0,1]
	v_pk_fma_f32 v[110:111], v[110:111], v[220:221], v[146:147] op_sel_hi:[1,0,1]
	v_pk_fma_f32 v[96:97], v[112:113], v[144:145], v[96:97] op_sel_hi:[1,0,1]
	s_waitcnt lgkmcnt(7)
	v_add_u32_e32 v112, s21, v131
	v_pk_fma_f32 v[98:99], v[114:115], v[144:145], v[98:99] op_sel_hi:[1,0,1]
	v_pk_fma_f32 v[100:101], v[116:117], v[144:145], v[100:101] op_sel_hi:[1,0,1]
	v_pk_fma_f32 v[102:103], v[118:119], v[144:145], v[102:103] op_sel_hi:[1,0,1]
	v_pk_fma_f32 v[104:105], v[120:121], v[144:145], v[104:105] op_sel_hi:[1,0,1]
	v_pk_fma_f32 v[106:107], v[122:123], v[144:145], v[106:107] op_sel_hi:[1,0,1]
	v_pk_fma_f32 v[108:109], v[124:125], v[144:145], v[108:109] op_sel_hi:[1,0,1]
	v_pk_fma_f32 v[110:111], v[126:127], v[144:145], v[110:111] op_sel_hi:[1,0,1]
	s_waitcnt lgkmcnt(6)
	v_add_u32_e32 v113, s21, v135
	s_waitcnt lgkmcnt(5)
	v_add_u32_e32 v114, s21, v139
	s_waitcnt lgkmcnt(4)
	v_add_u32_e32 v115, s21, v143
	s_waitcnt lgkmcnt(3)
	v_add_u32_e32 v116, s21, v153
	s_waitcnt lgkmcnt(2)
	v_add_u32_e32 v117, s21, v154
	s_waitcnt lgkmcnt(1)
	v_add_u32_e32 v118, s21, v155
	s_waitcnt lgkmcnt(0)
	v_add_u32_e32 v119, s21, v152
	v_pk_fma_f32 v[64:65], v[64:65], v[222:223], v[96:97] op_sel_hi:[1,0,1]
	v_mad_u32_u24 v96, v112, s16, v160
	v_cvt_scalef32_pk32_f32_fp6 v[32:63], v[186:191], 1.0
	v_cvt_scalef32_pk32_f32_fp6 v[0:31], v[192:197], 1.0
	v_mov_b32_e32 v146, v223
	v_pk_fma_f32 v[66:67], v[66:67], v[222:223], v[98:99] op_sel_hi:[1,0,1]
	v_pk_fma_f32 v[68:69], v[68:69], v[222:223], v[100:101] op_sel_hi:[1,0,1]
	v_pk_fma_f32 v[70:71], v[70:71], v[222:223], v[102:103] op_sel_hi:[1,0,1]
	v_pk_fma_f32 v[72:73], v[72:73], v[222:223], v[104:105] op_sel_hi:[1,0,1]
	v_pk_fma_f32 v[74:75], v[74:75], v[222:223], v[106:107] op_sel_hi:[1,0,1]
	v_pk_fma_f32 v[76:77], v[76:77], v[222:223], v[108:109] op_sel_hi:[1,0,1]
	v_pk_fma_f32 v[78:79], v[78:79], v[222:223], v[110:111] op_sel_hi:[1,0,1]
	v_mad_u32_u24 v98, v113, s16, v160
	v_mad_u32_u24 v100, v114, s16, v160
	v_mad_u32_u24 v102, v115, s16, v160
	v_mad_u32_u24 v104, v116, s16, v160
	v_mad_u32_u24 v106, v117, s16, v160
	v_mad_u32_u24 v108, v118, s16, v160
	v_mad_u32_u24 v110, v119, s16, v160
	global_load_dwordx3 v[180:182], v96, s[2:3]
	global_load_dwordx3 v[226:228], v98, s[2:3]
	global_load_dwordx3 v[186:188], v100, s[2:3]
	global_load_dwordx3 v[230:232], v102, s[2:3]
	global_load_dwordx3 v[192:194], v104, s[2:3]
	global_load_dwordx3 v[234:236], v106, s[2:3]
	global_load_dwordx3 v[222:224], v108, s[2:3]
	global_load_dwordx3 v[238:240], v110, s[2:3]
	s_waitcnt vmcnt(14)
	v_mov_b32_e32 v201, v128
	v_mov_b32_e32 v202, v129
	v_mov_b32_e32 v203, v130
	s_waitcnt vmcnt(12)
	v_mov_b32_e32 v207, v132
	v_mov_b32_e32 v208, v133
	v_mov_b32_e32 v209, v134
	s_waitcnt vmcnt(10)
; #define P12_VISSUE(c_, i_, q_, D_X) do { _Pragma("unroll") for (int b = 0; b < 8; ++b) { const int idx = ((q_) * 8 + b) * 4 + eg; const unsigned ro = (unsigned)(c_) * 16384u + (unsigned)EL[(i_) * 128 + idx]; \
;           const v3u_ ld_ = *(const v3u_*)(V8 + (size_t)(ro * 192u + 12u * (unsigned)cl)); if (b & 1) D_X[b >> 1].hi = ld_; else D_X[b >> 1].lo = ld_; } } while (0)
; __device__ __forceinline__ void p12_peer(Frame& F) {
;     ...
;       v6u_ dA[4], dB[4];
;       P12_VISSUE(0, 0, 0, dA);
; _Pragma("nounroll")
;       for (int c = 0; c < 16; ++c) {
;           int lo_ = 16 * cl + 4 * eg; asm volatile("" : "+v"(lo_));
; _Pragma("nounroll")
;           for (int i = 0; i < 4; ++i) { const int t = F.gw + i * F.NGW;
;               f32x2 acc2[8];
; #pragma unroll
;               for (int m = 0; m < 8; ++m) acc2[m] = (f32x2){0.f, 0.f};
;               const v2u hb = *(const v2u*)(HN + ((size_t)t * D_ + (size_t)(unsigned)(256 * c + lo_)));
;               P12_VISSUE(c, i, 1, dB); asm volatile("" ::: "memory"); P12_VCOMP(i, 0, dA);
;               P12_VISSUE(c, i, 2, dA); asm volatile("" ::: "memory"); P12_VCOMP(i, 1, dB);
;               P12_VISSUE(c, i, 3, dB); asm volatile("" ::: "memory"); P12_VCOMP(i, 2, dA);
;               { const int in_ = i + 1 < 4 ? i + 1 : 0, cn_ = i + 1 < 4 ? c : (c + 1 < 16 ? c + 1 : 15); P12_VISSUE(cn_, in_, 0, dA); } asm volatile("" ::: "memory"); P12_VCOMP(i, 3, dB);
	v_mov_b32_e32 v213, v136
	v_mov_b32_e32 v214, v137
	v_mov_b32_e32 v215, v138
	s_waitcnt vmcnt(8)
	v_mov_b32_e32 v219, v140
	v_mov_b32_e32 v220, v141
	v_mov_b32_e32 v221, v142
	v_pk_fma_f32 v[64:65], v[80:81], v[146:147], v[64:65] op_sel_hi:[1,0,1]
	v_pk_fma_f32 v[66:67], v[82:83], v[146:147], v[66:67] op_sel_hi:[1,0,1]
	v_pk_fma_f32 v[68:69], v[84:85], v[146:147], v[68:69] op_sel_hi:[1,0,1]
	v_pk_fma_f32 v[70:71], v[86:87], v[146:147], v[70:71] op_sel_hi:[1,0,1]
	v_pk_fma_f32 v[72:73], v[88:89], v[146:147], v[72:73] op_sel_hi:[1,0,1]
	v_pk_fma_f32 v[74:75], v[90:91], v[146:147], v[74:75] op_sel_hi:[1,0,1]
	v_pk_fma_f32 v[76:77], v[92:93], v[146:147], v[76:77] op_sel_hi:[1,0,1]
	v_pk_fma_f32 v[78:79], v[94:95], v[146:147], v[78:79] op_sel_hi:[1,0,1]
	ds_read2_b32 v[196:197], v177 offset0:64 offset1:68
	v_mov_b32_e32 v184, v243
	ds_read2_b32 v[246:247], v177 offset0:72 offset1:76
	ds_read2_b32 v[248:249], v177 offset0:80 offset1:84
	ds_read2_b32 v[250:251], v177 offset0:88 offset1:92
	v_pk_fma_f32 v[32:33], v[32:33], v[242:243], v[64:65] op_sel_hi:[1,0,1]
	v_pk_fma_f32 v[34:35], v[34:35], v[242:243], v[66:67] op_sel_hi:[1,0,1]
	v_pk_fma_f32 v[36:37], v[36:37], v[242:243], v[68:69] op_sel_hi:[1,0,1]
	v_pk_fma_f32 v[38:39], v[38:39], v[242:243], v[70:71] op_sel_hi:[1,0,1]
	v_pk_fma_f32 v[40:41], v[40:41], v[242:243], v[72:73] op_sel_hi:[1,0,1]
	v_pk_fma_f32 v[42:43], v[42:43], v[242:243], v[74:75] op_sel_hi:[1,0,1]
	v_pk_fma_f32 v[44:45], v[44:45], v[242:243], v[76:77] op_sel_hi:[1,0,1]
	v_pk_fma_f32 v[46:47], v[46:47], v[242:243], v[78:79] op_sel_hi:[1,0,1]
	v_cvt_scalef32_pk32_f32_fp6 v[128:159], v[198:203], 1.0
	v_cvt_scalef32_pk32_f32_fp6 v[96:127], v[204:209], 1.0
	v_cvt_scalef32_pk32_f32_fp6 v[64:95], v[210:215], 1.0
	v_pk_fma_f32 v[198:199], v[48:49], v[184:185], v[32:33] op_sel_hi:[1,0,1]
	v_pk_fma_f32 v[200:201], v[50:51], v[184:185], v[34:35] op_sel_hi:[1,0,1]
	v_pk_fma_f32 v[202:203], v[52:53], v[184:185], v[36:37] op_sel_hi:[1,0,1]
	v_pk_fma_f32 v[204:205], v[54:55], v[184:185], v[38:39] op_sel_hi:[1,0,1]
	v_pk_fma_f32 v[206:207], v[56:57], v[184:185], v[40:41] op_sel_hi:[1,0,1]
	v_pk_fma_f32 v[208:209], v[58:59], v[184:185], v[42:43] op_sel_hi:[1,0,1]
	v_pk_fma_f32 v[210:211], v[60:61], v[184:185], v[44:45] op_sel_hi:[1,0,1]
	v_pk_fma_f32 v[184:185], v[62:63], v[184:185], v[46:47] op_sel_hi:[1,0,1]
	ds_read_u16 v183, v179 offset:16384
	ds_read_u16 v189, v179 offset:16392
	ds_read_u16 v191, v179 offset:16400
	ds_read_u16 v195, v179 offset:16408
	ds_read_u16 v212, v179 offset:16416
	ds_read_u16 v213, v179 offset:16424
	ds_read_u16 v214, v179 offset:16432
	ds_read_u16 v179, v179 offset:16440
	v_mov_b32_e32 v190, v245
	v_pk_fma_f32 v[0:1], v[0:1], v[244:245], v[198:199] op_sel_hi:[1,0,1]
	v_pk_fma_f32 v[2:3], v[2:3], v[244:245], v[200:201] op_sel_hi:[1,0,1]
	v_pk_fma_f32 v[4:5], v[4:5], v[244:245], v[202:203] op_sel_hi:[1,0,1]
	v_pk_fma_f32 v[6:7], v[6:7], v[244:245], v[204:205] op_sel_hi:[1,0,1]
	v_pk_fma_f32 v[8:9], v[8:9], v[244:245], v[206:207] op_sel_hi:[1,0,1]
	v_pk_fma_f32 v[10:11], v[10:11], v[244:245], v[208:209] op_sel_hi:[1,0,1]
	v_pk_fma_f32 v[12:13], v[12:13], v[244:245], v[210:211] op_sel_hi:[1,0,1]
	v_pk_fma_f32 v[14:15], v[14:15], v[244:245], v[184:185] op_sel_hi:[1,0,1]
	s_cselect_b32 s29, s22, s17
	s_waitcnt lgkmcnt(5)
	v_pk_fma_f32 v[0:1], v[16:17], v[190:191], v[0:1] op_sel_hi:[1,0,1]
	v_pk_fma_f32 v[2:3], v[18:19], v[190:191], v[2:3] op_sel_hi:[1,0,1]
	v_pk_fma_f32 v[4:5], v[20:21], v[190:191], v[4:5] op_sel_hi:[1,0,1]
	v_pk_fma_f32 v[6:7], v[22:23], v[190:191], v[6:7] op_sel_hi:[1,0,1]
	v_pk_fma_f32 v[8:9], v[24:25], v[190:191], v[8:9] op_sel_hi:[1,0,1]
	v_pk_fma_f32 v[10:11], v[26:27], v[190:191], v[10:11] op_sel_hi:[1,0,1]
	v_pk_fma_f32 v[12:13], v[28:29], v[190:191], v[12:13] op_sel_hi:[1,0,1]
	v_pk_fma_f32 v[14:15], v[30:31], v[190:191], v[14:15] op_sel_hi:[1,0,1]
	s_lshl_b64 s[14:15], s[12:13], 14
	s_lshl_b32 s13, s29, 14
	v_pk_fma_f32 v[0:1], v[128:129], v[196:197], v[0:1] op_sel_hi:[1,0,1]
	v_pk_fma_f32 v[2:3], v[130:131], v[196:197], v[2:3] op_sel_hi:[1,0,1]
	v_pk_fma_f32 v[4:5], v[132:133], v[196:197], v[4:5] op_sel_hi:[1,0,1]
	v_pk_fma_f32 v[6:7], v[134:135], v[196:197], v[6:7] op_sel_hi:[1,0,1]
	v_pk_fma_f32 v[8:9], v[136:137], v[196:197], v[8:9] op_sel_hi:[1,0,1]
	v_pk_fma_f32 v[10:11], v[138:139], v[196:197], v[10:11] op_sel_hi:[1,0,1]
	v_pk_fma_f32 v[12:13], v[140:141], v[196:197], v[12:13] op_sel_hi:[1,0,1]
	v_pk_fma_f32 v[14:15], v[142:143], v[196:197], v[14:15] op_sel_hi:[1,0,1]
	v_mov_b32_e32 v16, v197
	v_pk_fma_f32 v[0:1], v[144:145], v[16:17], v[0:1] op_sel_hi:[1,0,1]
	v_pk_fma_f32 v[2:3], v[146:147], v[16:17], v[2:3] op_sel_hi:[1,0,1]
	v_pk_fma_f32 v[4:5], v[148:149], v[16:17], v[4:5] op_sel_hi:[1,0,1]
	v_pk_fma_f32 v[6:7], v[150:151], v[16:17], v[6:7] op_sel_hi:[1,0,1]
	v_pk_fma_f32 v[8:9], v[152:153], v[16:17], v[8:9] op_sel_hi:[1,0,1]
	v_pk_fma_f32 v[10:11], v[154:155], v[16:17], v[10:11] op_sel_hi:[1,0,1]
	v_pk_fma_f32 v[12:13], v[156:157], v[16:17], v[12:13] op_sel_hi:[1,0,1]
	v_pk_fma_f32 v[14:15], v[158:159], v[16:17], v[14:15] op_sel_hi:[1,0,1]
	v_add_u32_e32 v16, s13, v183
	v_add_u32_e32 v19, s13, v189
	v_add_u32_e32 v21, s13, v191
	s_waitcnt lgkmcnt(4)
	v_add_u32_e32 v23, s13, v195
	s_waitcnt lgkmcnt(3)
	v_add_u32_e32 v30, s13, v212
	s_waitcnt lgkmcnt(2)
	v_add_u32_e32 v128, s13, v213
	s_waitcnt lgkmcnt(1)
	v_add_u32_e32 v129, s13, v214
	s_waitcnt lgkmcnt(0)
; #define P12_VISSUE(c_, i_, q_, D_X) do { _Pragma("unroll") for (int b = 0; b < 8; ++b) { const int idx = ((q_) * 8 + b) * 4 + eg; const unsigned ro = (unsigned)(c_) * 16384u + (unsigned)EL[(i_) * 128 + idx]; \
;           const v3u_ ld_ = *(const v3u_*)(V8 + (size_t)(ro * 192u + 12u * (unsigned)cl)); if (b & 1) D_X[b >> 1].hi = ld_; else D_X[b >> 1].lo = ld_; } } while (0)
; __device__ __forceinline__ void p12_peer(Frame& F) {
;     ...
;       v6u_ dA[4], dB[4];
;       P12_VISSUE(0, 0, 0, dA);
; _Pragma("nounroll")
;       for (int c = 0; c < 16; ++c) {
;           int lo_ = 16 * cl + 4 * eg; asm volatile("" : "+v"(lo_));
; _Pragma("nounroll")
;           for (int i = 0; i < 4; ++i) { const int t = F.gw + i * F.NGW;
;               f32x2 acc2[8];
; #pragma unroll
;               for (int m = 0; m < 8; ++m) acc2[m] = (f32x2){0.f, 0.f};
;               const v2u hb = *(const v2u*)(HN + ((size_t)t * D_ + (size_t)(unsigned)(256 * c + lo_)));
;               P12_VISSUE(c, i, 1, dB); asm volatile("" ::: "memory"); P12_VCOMP(i, 0, dA);
;               P12_VISSUE(c, i, 2, dA); asm volatile("" ::: "memory"); P12_VCOMP(i, 1, dB);
;               P12_VISSUE(c, i, 3, dB); asm volatile("" ::: "memory"); P12_VCOMP(i, 2, dA);
;               { const int in_ = i + 1 < 4 ? i + 1 : 0, cn_ = i + 1 < 4 ? c : (c + 1 < 16 ? c + 1 : 15); P12_VISSUE(cn_, in_, 0, dA); } asm volatile("" ::: "memory"); P12_VCOMP(i, 3, dB);
	v_add_u32_e32 v130, s13, v179
	v_mad_u32_u24 v16, v16, s16, v160
	v_pk_fma_f32 v[0:1], v[96:97], v[246:247], v[0:1] op_sel_hi:[1,0,1]
	v_pk_fma_f32 v[2:3], v[98:99], v[246:247], v[2:3] op_sel_hi:[1,0,1]
	v_pk_fma_f32 v[4:5], v[100:101], v[246:247], v[4:5] op_sel_hi:[1,0,1]
	v_mad_u32_u24 v24, v19, s16, v160
	v_mad_u32_u24 v26, v21, s16, v160
	v_mad_u32_u24 v28, v23, s16, v160
	v_mad_u32_u24 v30, v30, s16, v160
	v_mad_u32_u24 v96, v128, s16, v160
	v_mad_u32_u24 v98, v129, s16, v160
	v_mad_u32_u24 v100, v130, s16, v160
	global_load_dwordx3 v[134:136], v16, s[2:3]
	global_load_dwordx3 v[152:154], v24, s[2:3]
	global_load_dwordx3 v[128:130], v26, s[2:3]
	global_load_dwordx3 v[156:158], v28, s[2:3]
	global_load_dwordx3 v[140:142], v30, s[2:3]
	global_load_dwordx3 v[198:200], v96, s[2:3]
	global_load_dwordx3 v[146:148], v98, s[2:3]
	global_load_dwordx3 v[202:204], v100, s[2:3]
	v_mov_b32_e32 v18, v247
	v_pk_fma_f32 v[6:7], v[102:103], v[246:247], v[6:7] op_sel_hi:[1,0,1]
	v_pk_fma_f32 v[8:9], v[104:105], v[246:247], v[8:9] op_sel_hi:[1,0,1]
	v_pk_fma_f32 v[10:11], v[106:107], v[246:247], v[10:11] op_sel_hi:[1,0,1]
	v_pk_fma_f32 v[12:13], v[108:109], v[246:247], v[12:13] op_sel_hi:[1,0,1]
	v_pk_fma_f32 v[14:15], v[110:111], v[246:247], v[14:15] op_sel_hi:[1,0,1]
	s_waitcnt vmcnt(14)
	v_mov_b32_e32 v183, v226
	v_mov_b32_e32 v184, v227
	v_mov_b32_e32 v185, v228
	v_pk_fma_f32 v[0:1], v[112:113], v[18:19], v[0:1] op_sel_hi:[1,0,1]
	v_pk_fma_f32 v[2:3], v[114:115], v[18:19], v[2:3] op_sel_hi:[1,0,1]
	v_pk_fma_f32 v[4:5], v[116:117], v[18:19], v[4:5] op_sel_hi:[1,0,1]
	v_pk_fma_f32 v[6:7], v[118:119], v[18:19], v[6:7] op_sel_hi:[1,0,1]
	v_pk_fma_f32 v[8:9], v[120:121], v[18:19], v[8:9] op_sel_hi:[1,0,1]
	v_pk_fma_f32 v[10:11], v[122:123], v[18:19], v[10:11] op_sel_hi:[1,0,1]
	v_pk_fma_f32 v[12:13], v[124:125], v[18:19], v[12:13] op_sel_hi:[1,0,1]
	v_pk_fma_f32 v[14:15], v[126:127], v[18:19], v[14:15] op_sel_hi:[1,0,1]
	ds_read2_b32 v[214:215], v177 offset0:96 offset1:100
	v_mov_b32_e32 v20, v249
	v_pk_fma_f32 v[0:1], v[64:65], v[248:249], v[0:1] op_sel_hi:[1,0,1]
	v_pk_fma_f32 v[2:3], v[66:67], v[248:249], v[2:3] op_sel_hi:[1,0,1]
	v_pk_fma_f32 v[4:5], v[68:69], v[248:249], v[4:5] op_sel_hi:[1,0,1]
	v_pk_fma_f32 v[6:7], v[70:71], v[248:249], v[6:7] op_sel_hi:[1,0,1]
	v_pk_fma_f32 v[8:9], v[72:73], v[248:249], v[8:9] op_sel_hi:[1,0,1]
	v_pk_fma_f32 v[10:11], v[74:75], v[248:249], v[10:11] op_sel_hi:[1,0,1]
	v_pk_fma_f32 v[12:13], v[76:77], v[248:249], v[12:13] op_sel_hi:[1,0,1]
	v_pk_fma_f32 v[14:15], v[78:79], v[248:249], v[14:15] op_sel_hi:[1,0,1]
	s_waitcnt vmcnt(12)
	v_mov_b32_e32 v189, v230
	v_mov_b32_e32 v190, v231
	v_mov_b32_e32 v191, v232
	v_cvt_scalef32_pk32_f32_fp6 v[32:63], v[216:221], 1.0
	v_pk_fma_f32 v[0:1], v[80:81], v[20:21], v[0:1] op_sel_hi:[1,0,1]
	v_pk_fma_f32 v[2:3], v[82:83], v[20:21], v[2:3] op_sel_hi:[1,0,1]
	v_pk_fma_f32 v[4:5], v[84:85], v[20:21], v[4:5] op_sel_hi:[1,0,1]
	v_pk_fma_f32 v[6:7], v[86:87], v[20:21], v[6:7] op_sel_hi:[1,0,1]
	v_pk_fma_f32 v[8:9], v[88:89], v[20:21], v[8:9] op_sel_hi:[1,0,1]
	v_pk_fma_f32 v[10:11], v[90:91], v[20:21], v[10:11] op_sel_hi:[1,0,1]
	v_pk_fma_f32 v[12:13], v[92:93], v[20:21], v[12:13] op_sel_hi:[1,0,1]
	v_pk_fma_f32 v[14:15], v[94:95], v[20:21], v[14:15] op_sel_hi:[1,0,1]
	ds_read2_b32 v[216:217], v177 offset0:104 offset1:108
	v_mov_b32_e32 v22, v251
	v_pk_fma_f32 v[0:1], v[32:33], v[250:251], v[0:1] op_sel_hi:[1,0,1]
	v_pk_fma_f32 v[2:3], v[34:35], v[250:251], v[2:3] op_sel_hi:[1,0,1]
	v_pk_fma_f32 v[4:5], v[36:37], v[250:251], v[4:5] op_sel_hi:[1,0,1]
	v_pk_fma_f32 v[6:7], v[38:39], v[250:251], v[6:7] op_sel_hi:[1,0,1]
	v_pk_fma_f32 v[8:9], v[40:41], v[250:251], v[8:9] op_sel_hi:[1,0,1]
	v_pk_fma_f32 v[10:11], v[42:43], v[250:251], v[10:11] op_sel_hi:[1,0,1]
	v_pk_fma_f32 v[12:13], v[44:45], v[250:251], v[12:13] op_sel_hi:[1,0,1]
	v_pk_fma_f32 v[14:15], v[46:47], v[250:251], v[14:15] op_sel_hi:[1,0,1]
	s_waitcnt vmcnt(10)
	v_mov_b32_e32 v195, v234
	v_mov_b32_e32 v196, v235
	v_mov_b32_e32 v197, v236
	v_mov_b32_e32 v162, v176
	v_pk_fma_f32 v[132:133], v[48:49], v[22:23], v[0:1] op_sel_hi:[1,0,1]
	v_pk_fma_f32 v[138:139], v[50:51], v[22:23], v[2:3] op_sel_hi:[1,0,1]
	v_pk_fma_f32 v[144:145], v[52:53], v[22:23], v[4:5] op_sel_hi:[1,0,1]
	v_pk_fma_f32 v[150:151], v[54:55], v[22:23], v[6:7] op_sel_hi:[1,0,1]
	v_pk_fma_f32 v[206:207], v[56:57], v[22:23], v[8:9] op_sel_hi:[1,0,1]
	v_pk_fma_f32 v[208:209], v[58:59], v[22:23], v[10:11] op_sel_hi:[1,0,1]
	v_pk_fma_f32 v[210:211], v[60:61], v[22:23], v[12:13] op_sel_hi:[1,0,1]
	v_pk_fma_f32 v[212:213], v[62:63], v[22:23], v[14:15] op_sel_hi:[1,0,1]
	s_waitcnt vmcnt(8)
	v_mov_b32_e32 v225, v238
	v_mov_b32_e32 v226, v239
	v_mov_b32_e32 v227, v240
	ds_read2_b32 v[218:219], v177 offset0:112 offset1:116
	v_cvt_scalef32_pk32_f32_fp6 v[96:127], v[180:185], 1.0
	s_add_u32 s14, s26, s14
	ds_read2_b32 v[220:221], v177 offset0:120 offset1:124
	s_waitcnt lgkmcnt(3)
; #define P12_VISSUE(c_, i_, q_, D_X) do { _Pragma("unroll") for (int b = 0; b < 8; ++b) { const int idx = ((q_) * 8 + b) * 4 + eg; const unsigned ro = (unsigned)(c_) * 16384u + (unsigned)EL[(i_) * 128 + idx]; \
;           const v3u_ ld_ = *(const v3u_*)(V8 + (size_t)(ro * 192u + 12u * (unsigned)cl)); if (b & 1) D_X[b >> 1].hi = ld_; else D_X[b >> 1].lo = ld_; } } while (0)
; __device__ __forceinline__ void p12_peer(Frame& F) {
;     ...
;               { const int in_ = i + 1 < 4 ? i + 1 : 0, cn_ = i + 1 < 4 ? c : (c + 1 < 16 ? c + 1 : 15); P12_VISSUE(cn_, in_, 0, dA); } asm volatile("" ::: "memory"); P12_VCOMP(i, 3, dB);
;               float r8[8], r4[4];
; #pragma unroll
;               for (int m = 0; m < 8; ++m) { const float lo_v = (m & 1) ? acc2[m >> 1].y : acc2[m >> 1].x, hi_v = (m & 1) ? acc2[4 + (m >> 1)].y : acc2[4 + (m >> 1)].x;
;                   const float keep = hi5 ? hi_v : lo_v, send = hi5 ? lo_v : hi_v;
;                   r8[m] = keep + __builtin_bit_cast(float, __builtin_amdgcn_ds_bpermute((F.lane ^ 32) << 2, __builtin_bit_cast(int, send))); }
; #pragma unroll
;               for (int m = 0; m < 4; ++m) { const float keep = hi4 ? r8[4 + m] : r8[m], send = hi4 ? r8[m] : r8[4 + m];
;                   r4[m] = keep + __builtin_bit_cast(float, __builtin_amdgcn_ds_bpermute((F.lane ^ 16) << 2, __builtin_bit_cast(int, send))); }
;               int lo3_ = lo_; asm volatile("" : "+v"(lo3_));
;               const size_t col = (size_t)t * D_ + (size_t)(unsigned)(256 * c + lo3_);
	v_pk_fma_f32 v[96:97], v[96:97], v[214:215], v[132:133] op_sel_hi:[1,0,1]
	v_pk_fma_f32 v[98:99], v[98:99], v[214:215], v[138:139] op_sel_hi:[1,0,1]
	v_pk_fma_f32 v[100:101], v[100:101], v[214:215], v[144:145] op_sel_hi:[1,0,1]
	v_pk_fma_f32 v[102:103], v[102:103], v[214:215], v[150:151] op_sel_hi:[1,0,1]
	v_pk_fma_f32 v[104:105], v[104:105], v[214:215], v[206:207] op_sel_hi:[1,0,1]
	v_pk_fma_f32 v[106:107], v[106:107], v[214:215], v[208:209] op_sel_hi:[1,0,1]
	v_pk_fma_f32 v[108:109], v[108:109], v[214:215], v[210:211] op_sel_hi:[1,0,1]
	v_pk_fma_f32 v[110:111], v[110:111], v[214:215], v[212:213] op_sel_hi:[1,0,1]
	v_mov_b32_e32 v132, v215
	s_addc_u32 s15, s27, s15
	v_cvt_scalef32_pk32_f32_fp6 v[64:95], v[186:191], 1.0
	v_add_u32_e32 v162, s18, v162
	v_pk_fma_f32 v[96:97], v[112:113], v[132:133], v[96:97] op_sel_hi:[1,0,1]
	v_pk_fma_f32 v[98:99], v[114:115], v[132:133], v[98:99] op_sel_hi:[1,0,1]
	v_pk_fma_f32 v[100:101], v[116:117], v[132:133], v[100:101] op_sel_hi:[1,0,1]
	v_pk_fma_f32 v[102:103], v[118:119], v[132:133], v[102:103] op_sel_hi:[1,0,1]
	v_pk_fma_f32 v[104:105], v[120:121], v[132:133], v[104:105] op_sel_hi:[1,0,1]
	v_pk_fma_f32 v[106:107], v[122:123], v[132:133], v[106:107] op_sel_hi:[1,0,1]
	v_pk_fma_f32 v[108:109], v[124:125], v[132:133], v[108:109] op_sel_hi:[1,0,1]
	v_pk_fma_f32 v[110:111], v[126:127], v[132:133], v[110:111] op_sel_hi:[1,0,1]
	v_lshl_add_u64 v[180:181], v[162:163], 2, s[14:15]
	s_waitcnt lgkmcnt(2)
	v_mov_b32_e32 v162, v217
	v_pk_fma_f32 v[64:65], v[64:65], v[216:217], v[96:97] op_sel_hi:[1,0,1]
	v_pk_fma_f32 v[66:67], v[66:67], v[216:217], v[98:99] op_sel_hi:[1,0,1]
	v_pk_fma_f32 v[68:69], v[68:69], v[216:217], v[100:101] op_sel_hi:[1,0,1]
	v_pk_fma_f32 v[70:71], v[70:71], v[216:217], v[102:103] op_sel_hi:[1,0,1]
	v_pk_fma_f32 v[72:73], v[72:73], v[216:217], v[104:105] op_sel_hi:[1,0,1]
	v_pk_fma_f32 v[74:75], v[74:75], v[216:217], v[106:107] op_sel_hi:[1,0,1]
	v_pk_fma_f32 v[76:77], v[76:77], v[216:217], v[108:109] op_sel_hi:[1,0,1]
	v_pk_fma_f32 v[78:79], v[78:79], v[216:217], v[110:111] op_sel_hi:[1,0,1]
	v_cvt_scalef32_pk32_f32_fp6 v[32:63], v[192:197], 1.0
	v_pk_fma_f32 v[64:65], v[80:81], v[162:163], v[64:65] op_sel_hi:[1,0,1]
	v_pk_fma_f32 v[66:67], v[82:83], v[162:163], v[66:67] op_sel_hi:[1,0,1]
	v_pk_fma_f32 v[68:69], v[84:85], v[162:163], v[68:69] op_sel_hi:[1,0,1]
	v_pk_fma_f32 v[70:71], v[86:87], v[162:163], v[70:71] op_sel_hi:[1,0,1]
	v_pk_fma_f32 v[72:73], v[88:89], v[162:163], v[72:73] op_sel_hi:[1,0,1]
	v_pk_fma_f32 v[74:75], v[90:91], v[162:163], v[74:75] op_sel_hi:[1,0,1]
	v_pk_fma_f32 v[76:77], v[92:93], v[162:163], v[76:77] op_sel_hi:[1,0,1]
	v_pk_fma_f32 v[78:79], v[94:95], v[162:163], v[78:79] op_sel_hi:[1,0,1]
	s_waitcnt lgkmcnt(1)
	v_mov_b32_e32 v182, v219
	v_pk_fma_f32 v[32:33], v[32:33], v[218:219], v[64:65] op_sel_hi:[1,0,1]
	v_pk_fma_f32 v[34:35], v[34:35], v[218:219], v[66:67] op_sel_hi:[1,0,1]
	v_pk_fma_f32 v[36:37], v[36:37], v[218:219], v[68:69] op_sel_hi:[1,0,1]
	v_pk_fma_f32 v[38:39], v[38:39], v[218:219], v[70:71] op_sel_hi:[1,0,1]
	v_pk_fma_f32 v[40:41], v[40:41], v[218:219], v[72:73] op_sel_hi:[1,0,1]
	v_pk_fma_f32 v[42:43], v[42:43], v[218:219], v[74:75] op_sel_hi:[1,0,1]
	v_pk_fma_f32 v[44:45], v[44:45], v[218:219], v[76:77] op_sel_hi:[1,0,1]
	v_pk_fma_f32 v[46:47], v[46:47], v[218:219], v[78:79] op_sel_hi:[1,0,1]
	v_cvt_scalef32_pk32_f32_fp6 v[0:31], v[222:227], 1.0
	v_pk_fma_f32 v[32:33], v[48:49], v[182:183], v[32:33] op_sel_hi:[1,0,1]
	v_pk_fma_f32 v[34:35], v[50:51], v[182:183], v[34:35] op_sel_hi:[1,0,1]
	v_pk_fma_f32 v[36:37], v[52:53], v[182:183], v[36:37] op_sel_hi:[1,0,1]
	v_pk_fma_f32 v[38:39], v[54:55], v[182:183], v[38:39] op_sel_hi:[1,0,1]
	v_pk_fma_f32 v[40:41], v[56:57], v[182:183], v[40:41] op_sel_hi:[1,0,1]
	v_pk_fma_f32 v[42:43], v[58:59], v[182:183], v[42:43] op_sel_hi:[1,0,1]
	v_pk_fma_f32 v[44:45], v[60:61], v[182:183], v[44:45] op_sel_hi:[1,0,1]
	v_pk_fma_f32 v[46:47], v[62:63], v[182:183], v[46:47] op_sel_hi:[1,0,1]
	s_waitcnt lgkmcnt(0)
	v_mov_b32_e32 v184, v221
	v_pk_fma_f32 v[0:1], v[0:1], v[220:221], v[32:33] op_sel_hi:[1,0,1]
	v_pk_fma_f32 v[2:3], v[2:3], v[220:221], v[34:35] op_sel_hi:[1,0,1]
	v_pk_fma_f32 v[4:5], v[4:5], v[220:221], v[36:37] op_sel_hi:[1,0,1]
	v_pk_fma_f32 v[6:7], v[6:7], v[220:221], v[38:39] op_sel_hi:[1,0,1]
	v_pk_fma_f32 v[8:9], v[8:9], v[220:221], v[40:41] op_sel_hi:[1,0,1]
	v_pk_fma_f32 v[10:11], v[10:11], v[220:221], v[42:43] op_sel_hi:[1,0,1]
	v_pk_fma_f32 v[12:13], v[12:13], v[220:221], v[44:45] op_sel_hi:[1,0,1]
	v_pk_fma_f32 v[14:15], v[14:15], v[220:221], v[46:47] op_sel_hi:[1,0,1]
	v_pk_fma_f32 v[0:1], v[16:17], v[184:185], v[0:1] op_sel_hi:[1,0,1]
	v_pk_fma_f32 v[2:3], v[18:19], v[184:185], v[2:3] op_sel_hi:[1,0,1]
	v_pk_fma_f32 v[4:5], v[20:21], v[184:185], v[4:5] op_sel_hi:[1,0,1]
	v_pk_fma_f32 v[6:7], v[22:23], v[184:185], v[6:7] op_sel_hi:[1,0,1]
	v_pk_fma_f32 v[8:9], v[24:25], v[184:185], v[8:9] op_sel_hi:[1,0,1]
	v_pk_fma_f32 v[10:11], v[26:27], v[184:185], v[10:11] op_sel_hi:[1,0,1]
	v_pk_fma_f32 v[12:13], v[28:29], v[184:185], v[12:13] op_sel_hi:[1,0,1]
	v_pk_fma_f32 v[14:15], v[30:31], v[184:185], v[14:15] op_sel_hi:[1,0,1]
	v_cndmask_b32_e32 v18, v0, v8, vcc
	v_cndmask_b32_e32 v19, v1, v9, vcc
	v_cndmask_b32_e32 v20, v2, v10, vcc
	v_cndmask_b32_e32 v21, v3, v11, vcc
	v_cndmask_b32_e32 v22, v4, v12, vcc
	v_cndmask_b32_e32 v23, v5, v13, vcc
	v_cndmask_b32_e32 v24, v6, v14, vcc
	v_cndmask_b32_e32 v25, v7, v15, vcc
	v_cndmask_b32_e32 v17, v10, v2, vcc
	v_cndmask_b32_e32 v16, v8, v0, vcc
	v_cndmask_b32_e32 v3, v11, v3, vcc
	v_cndmask_b32_e32 v2, v9, v1, vcc
	v_cndmask_b32_e32 v1, v14, v6, vcc
	v_cndmask_b32_e32 v0, v12, v4, vcc
	v_cndmask_b32_e32 v6, v13, v5, vcc
	ds_bpermute_b32 v4, v171, v18
	ds_bpermute_b32 v8, v171, v19
	ds_bpermute_b32 v5, v171, v20
	ds_bpermute_b32 v9, v171, v21
	ds_bpermute_b32 v10, v171, v22
	ds_bpermute_b32 v12, v171, v23
	ds_bpermute_b32 v11, v171, v24
	ds_bpermute_b32 v13, v171, v25
	v_cndmask_b32_e32 v7, v15, v7, vcc
	s_waitcnt lgkmcnt(5)
; __device__ __forceinline__ int fresh_lane() { int l; asm volatile("v_mbcnt_lo_u32_b32 %0, -1, 0\n\tv_mbcnt_hi_u32_b32 %0, -1, %0" : "=v"(l)); return l; }
; __device__ __forceinline__ float bflo(unsigned w) { return __uint_as_float(w << 16); }
; __device__ __forceinline__ float bfhi(unsigned w) { return __uint_as_float(w & 0xffff0000u); }
; __device__ __forceinline__ float wave_sum(float v) { v = dpp_add16(v); return (rdlane(v, 0) + rdlane(v, 16)) + (rdlane(v, 32) + rdlane(v, 48)); }
; __device__ __forceinline__ void p12_peer(Frame& F) {
;     ...
;               for (int m = 0; m < 4; ++m) { const float keep = hi4 ? r8[4 + m] : r8[m], send = hi4 ? r8[m] : r8[4 + m];
;                   r4[m] = keep + __builtin_bit_cast(float, __builtin_amdgcn_ds_bpermute((F.lane ^ 16) << 2, __builtin_bit_cast(int, send))); }
;               int lo3_ = lo_; asm volatile("" : "+v"(lo3_));
;               const size_t col = (size_t)t * D_ + (size_t)(unsigned)(256 * c + lo3_);
;               const f32x4 o = {r4[0] + bflo(hb.x), r4[1] + bfhi(hb.x), r4[2] + bflo(hb.y), r4[3] + bfhi(hb.y)};
;               SSQ[i * 64 + F.lane] += (o.x * o.x + o.y * o.y) + (o.z * o.z + o.w * o.w);
;               *(f32x4*)(F.out + col) = o;
;           }
;       }
;     ...
;       __builtin_amdgcn_fence(__ATOMIC_SEQ_CST, "agent");
;       const int l2_ = fresh_lane(), lo2_ = 16 * (l2_ & 15) + 4 * (l2_ >> 4);
; #pragma unroll
;       for (int i = 0; i < 4; ++i) { const int t = F.gw + i * F.NGW;
;           const float rs = 1.0f / sqrtf(wave_sum(SSQ[i * 64 + l2_]) * (1.f / D_) + 1e-6f);
; _Pragma("nounroll")
;           for (int c0 = 0; c0 < 16; c0 += 8) {
; #pragma unroll
;               for (int c = c0; c < c0 + 8; ++c) { const size_t col = (size_t)t * D_ + (size_t)(unsigned)(256 * c + lo2_); const f32x4 gn = *(const f32x4*)(lnf + (256 * c + lo2_));
;                   const f32x4 o = *(const f32x4*)(F.out + col);
;                   *(f32x4*)(F.out + col) = (f32x4){o.x * rs * gn.x, o.y * rs * gn.y, o.z * rs * gn.z, o.w * rs * gn.w}; }
;               asm volatile("" ::: "memory"); } }
	v_pk_add_f32 v[4:5], v[16:17], v[4:5]
	s_waitcnt lgkmcnt(4)
	v_pk_add_f32 v[2:3], v[2:3], v[8:9]
	s_waitcnt lgkmcnt(1)
	v_pk_add_f32 v[0:1], v[0:1], v[10:11]
	s_waitcnt lgkmcnt(0)
	v_pk_add_f32 v[6:7], v[6:7], v[12:13]
	v_cndmask_b32_e64 v10, v4, v0, s[0:1]
	v_cndmask_b32_e64 v11, v2, v6, s[0:1]
	v_cndmask_b32_e64 v9, v1, v5, s[0:1]
	v_cndmask_b32_e64 v8, v0, v4, s[0:1]
	v_cndmask_b32_e64 v5, v5, v1, s[0:1]
	v_cndmask_b32_e64 v0, v6, v2, s[0:1]
	v_cndmask_b32_e64 v6, v3, v7, s[0:1]
	v_cndmask_b32_e64 v1, v7, v3, s[0:1]
	ds_bpermute_b32 v2, v170, v10
	ds_bpermute_b32 v4, v170, v11
	ds_bpermute_b32 v3, v170, v5
	ds_bpermute_b32 v5, v170, v6
	v_add_u32_e32 v178, s28, v174
	ds_read_b32 v155, v178
	s_addk_i32 s28, 0x100
	s_waitcnt lgkmcnt(2)
	v_pk_add_f32 v[2:3], v[8:9], v[2:3]
	s_waitcnt lgkmcnt(1)
	v_pk_add_f32 v[0:1], v[0:1], v[4:5]
	v_pk_add_f32 v[4:5], v[2:3], v[166:167]
	v_pk_add_f32 v[2:3], v[0:1], v[168:169]
	v_mov_b32_e32 v0, v4
	v_pk_mul_f32 v[6:7], v[2:3], v[2:3]
	v_mov_b32_e32 v1, v2
	v_mov_b32_e32 v2, v5
	v_pk_fma_f32 v[4:5], v[4:5], v[4:5], v[6:7]
	s_addk_i32 s23, 0x80
	s_add_i32 s12, s12, s34
	global_store_dwordx4 v[180:181], v[0:3], off
	s_cmpk_eq_i32 s28, 0x400
	v_add_u32_e32 v177, 0x200, v177
	v_add_f32_e32 v0, v4, v5
	s_waitcnt vmcnt(1)
	v_mov_b32_e32 v149, v202
	v_mov_b32_e32 v150, v203
	v_mov_b32_e32 v151, v204
	v_mov_b32_e32 v143, v198
	v_mov_b32_e32 v144, v199
	v_mov_b32_e32 v145, v200
	v_mov_b32_e32 v131, v156
	v_mov_b32_e32 v132, v157
	v_mov_b32_e32 v133, v158
	v_mov_b32_e32 v137, v152
	v_mov_b32_e32 v138, v153
	v_mov_b32_e32 v139, v154
	s_waitcnt lgkmcnt(0)
	v_add_f32_e32 v0, v155, v0
	ds_write_b32 v178, v0
	s_cbranch_scc0 .LBB0_3403
	s_cmp_eq_u32 s19, 16
	s_mov_b32 s17, s19
	s_cbranch_scc0 .LBB0_3402
	s_waitcnt vmcnt(0) lgkmcnt(0)
	buffer_inv sc1
	v_mbcnt_lo_u32_b32 v0, -1, 0
	v_mbcnt_hi_u32_b32 v0, -1, v0
	v_lshl_add_u32 v7, v0, 2, s20
	v_and_b32_e32 v2, 15, v0
	v_lshrrev_b32_e32 v3, 4, v0
	v_lshlrev_b32_e32 v2, 6, v2
	v_lshl_add_u32 v6, v3, 4, v2
	v_add_u32_e32 v10, 0x1000, v6
	v_add_u32_e32 v11, 0x2000, v6
	v_add_u32_e32 v12, 0x3000, v6
	s_lshl_b64 s[0:1], s[94:95], 14
	s_add_u32 s12, s26, s0
	s_addc_u32 s13, s27, s1
	s_lshl_b64 s[0:1], s[4:5], 14
	s_add_u32 s14, s26, s0
	s_addc_u32 s15, s27, s1
	s_lshl_b64 s[0:1], s[8:9], 14
	s_add_u32 s16, s26, s0
	s_addc_u32 s17, s27, s1
	s_lshl_b64 s[0:1], s[10:11], 14
	s_add_u32 s18, s26, s0
	s_addc_u32 s19, s27, s1
	global_load_dwordx4 v[60:63], v6, s[24:25] offset:0
	global_load_dwordx4 v[64:67], v6, s[24:25] offset:1024
	global_load_dwordx4 v[68:71], v6, s[24:25] offset:2048
	global_load_dwordx4 v[72:75], v6, s[24:25] offset:3072
	global_load_dwordx4 v[76:79], v10, s[24:25] offset:0
	global_load_dwordx4 v[80:83], v10, s[24:25] offset:1024
	global_load_dwordx4 v[84:87], v10, s[24:25] offset:2048
	global_load_dwordx4 v[88:91], v10, s[24:25] offset:3072
	global_load_dwordx4 v[92:95], v11, s[24:25] offset:0
	global_load_dwordx4 v[96:99], v11, s[24:25] offset:1024
	global_load_dwordx4 v[100:103], v11, s[24:25] offset:2048
	global_load_dwordx4 v[104:107], v11, s[24:25] offset:3072
	global_load_dwordx4 v[108:111], v12, s[24:25] offset:0
	global_load_dwordx4 v[112:115], v12, s[24:25] offset:1024
	global_load_dwordx4 v[116:119], v12, s[24:25] offset:2048
	global_load_dwordx4 v[120:123], v12, s[24:25] offset:3072
	global_load_dwordx4 v[124:127], v6, s[12:13] offset:0
	global_load_dwordx4 v[128:131], v6, s[12:13] offset:1024
	global_load_dwordx4 v[132:135], v6, s[12:13] offset:2048
	global_load_dwordx4 v[136:139], v6, s[12:13] offset:3072
	global_load_dwordx4 v[140:143], v10, s[12:13] offset:0
	global_load_dwordx4 v[144:147], v10, s[12:13] offset:1024
	global_load_dwordx4 v[148:151], v10, s[12:13] offset:2048
	global_load_dwordx4 v[152:155], v10, s[12:13] offset:3072
	global_load_dwordx4 v[156:159], v11, s[12:13] offset:0
	global_load_dwordx4 v[160:163], v11, s[12:13] offset:1024
	global_load_dwordx4 v[164:167], v11, s[12:13] offset:2048
	global_load_dwordx4 v[168:171], v11, s[12:13] offset:3072
	global_load_dwordx4 v[172:175], v12, s[12:13] offset:0
	global_load_dwordx4 v[176:179], v12, s[12:13] offset:1024
	global_load_dwordx4 v[180:183], v12, s[12:13] offset:2048
	global_load_dwordx4 v[184:187], v12, s[12:13] offset:3072
	global_load_dwordx4 v[188:191], v6, s[14:15] offset:0
	global_load_dwordx4 v[192:195], v6, s[14:15] offset:1024
	global_load_dwordx4 v[196:199], v6, s[14:15] offset:2048
	global_load_dwordx4 v[200:203], v6, s[14:15] offset:3072
	global_load_dwordx4 v[204:207], v10, s[14:15] offset:0
	global_load_dwordx4 v[208:211], v10, s[14:15] offset:1024
	global_load_dwordx4 v[212:215], v10, s[14:15] offset:2048
	global_load_dwordx4 v[216:219], v10, s[14:15] offset:3072
	global_load_dwordx4 v[220:223], v11, s[14:15] offset:0
	global_load_dwordx4 v[224:227], v11, s[14:15] offset:1024
	global_load_dwordx4 v[228:231], v11, s[14:15] offset:2048
	global_load_dwordx4 v[232:235], v11, s[14:15] offset:3072
	global_load_dwordx4 v[236:239], v12, s[14:15] offset:0
	global_load_dwordx4 v[240:243], v12, s[14:15] offset:1024
	global_load_dwordx4 v[244:247], v12, s[14:15] offset:2048
	global_load_dwordx4 v[248:251], v12, s[14:15] offset:3072
	ds_read_b32 v1, v7 offset:4096
	s_waitcnt lgkmcnt(0)
; __device__ __forceinline__ int fresh_lane() { int l; asm volatile("v_mbcnt_lo_u32_b32 %0, -1, 0\n\tv_mbcnt_hi_u32_b32 %0, -1, %0" : "=v"(l)); return l; }
; __device__ __forceinline__ float wave_sum(float v) { v = dpp_add16(v); return (rdlane(v, 0) + rdlane(v, 16)) + (rdlane(v, 32) + rdlane(v, 48)); }
; __device__ __forceinline__ void p12_peer(Frame& F) {
;     ...
;       const int l2_ = fresh_lane(), lo2_ = 16 * (l2_ & 15) + 4 * (l2_ >> 4);
; #pragma unroll
;       for (int i = 0; i < 4; ++i) { const int t = F.gw + i * F.NGW;
;           const float rs = 1.0f / sqrtf(wave_sum(SSQ[i * 64 + l2_]) * (1.f / D_) + 1e-6f);
	v_add_f32_dpp v1, v1, v1 quad_perm:[1,0,3,2] row_mask:0xf bank_mask:0xf bound_ctrl:1
	s_nop 1
	v_add_f32_dpp v1, v1, v1 quad_perm:[2,3,0,1] row_mask:0xf bank_mask:0xf bound_ctrl:1
	s_nop 1
	v_add_f32_dpp v1, v1, v1 row_half_mirror row_mask:0xf bank_mask:0xf bound_ctrl:1
	s_nop 1
	v_add_f32_dpp v1, v1, v1 row_mirror row_mask:0xf bank_mask:0xf bound_ctrl:1
	s_nop 0
	v_readlane_b32 s1, v1, 16
	v_readlane_b32 s0, v1, 0
	s_nop 0
	v_mov_b32_e32 v3, s1
	v_readlane_b32 s1, v1, 48
	v_add_f32_e32 v3, s0, v3
	v_readlane_b32 s0, v1, 32
	v_mov_b32_e32 v1, s1
	s_nop 0
	v_add_f32_e32 v1, s0, v1
	v_add_f32_e32 v1, v3, v1
	v_mov_b32_e32 v3, 0x358637bd
	v_fmac_f32_e32 v3, 0x39800000, v1
	s_mov_b32 s0, 0xf800000
	v_mul_f32_e32 v1, 0x4f800000, v3
	v_cmp_gt_f32_e32 vcc, s0, v3
	s_nop 1
	v_cndmask_b32_e32 v1, v3, v1, vcc
	v_sqrt_f32_e32 v3, v1
	s_nop 0
	v_add_u32_e32 v4, -1, v3
	v_fma_f32 v5, -v4, v3, v1
	v_cmp_ge_f32_e64 s[0:1], 0, v5
	v_add_u32_e32 v5, 1, v3
	s_nop 0
	v_cndmask_b32_e64 v4, v3, v4, s[0:1]
	v_fma_f32 v3, -v5, v3, v1
	v_cmp_lt_f32_e64 s[0:1], 0, v3
	s_nop 1
	v_cndmask_b32_e64 v3, v4, v5, s[0:1]
	v_mul_f32_e32 v4, 0x37800000, v3
	v_cndmask_b32_e32 v3, v3, v4, vcc
	v_mov_b32_e32 v4, 0x260
	v_cmp_class_f32_e32 vcc, v1, v4
	s_nop 1
	v_cndmask_b32_e32 v3, v3, v1, vcc
	v_div_scale_f32 v4, s[0:1], v3, v3, 1.0
	v_rcp_f32_e32 v5, v4
	s_nop 0
	v_fma_f32 v0, -v4, v5, 1.0
	v_fmac_f32_e32 v5, v0, v5
	v_div_scale_f32 v0, vcc, 1.0, v3, 1.0
	v_mul_f32_e32 v2, v0, v5
	v_fma_f32 v8, -v4, v2, v0
	v_fmac_f32_e32 v2, v8, v5
	v_fma_f32 v0, -v4, v2, v0
	v_div_fmas_f32 v0, v0, v5, v2
	v_div_fixup_f32 v2, v0, v3, 1.0
	v_mov_b32_e32 v40, v2
	v_mov_b32_e32 v41, v2
	ds_read_b32 v1, v7 offset:4352
	s_waitcnt lgkmcnt(0)
	v_add_f32_dpp v1, v1, v1 quad_perm:[1,0,3,2] row_mask:0xf bank_mask:0xf bound_ctrl:1
	s_nop 1
	v_add_f32_dpp v1, v1, v1 quad_perm:[2,3,0,1] row_mask:0xf bank_mask:0xf bound_ctrl:1
	s_nop 1
	v_add_f32_dpp v1, v1, v1 row_half_mirror row_mask:0xf bank_mask:0xf bound_ctrl:1
	s_nop 1
	v_add_f32_dpp v1, v1, v1 row_mirror row_mask:0xf bank_mask:0xf bound_ctrl:1
	s_nop 0
	v_readlane_b32 s1, v1, 16
	v_readlane_b32 s0, v1, 0
	s_nop 0
	v_mov_b32_e32 v3, s1
	v_readlane_b32 s1, v1, 48
	v_add_f32_e32 v3, s0, v3
	v_readlane_b32 s0, v1, 32
	v_mov_b32_e32 v1, s1
	s_nop 0
	v_add_f32_e32 v1, s0, v1
	v_add_f32_e32 v1, v3, v1
	v_mov_b32_e32 v3, 0x358637bd
	v_fmac_f32_e32 v3, 0x39800000, v1
	s_mov_b32 s0, 0xf800000
	v_mul_f32_e32 v1, 0x4f800000, v3
	v_cmp_gt_f32_e32 vcc, s0, v3
	s_nop 1
	v_cndmask_b32_e32 v1, v3, v1, vcc
	v_sqrt_f32_e32 v3, v1
	s_nop 0
	v_add_u32_e32 v4, -1, v3
	v_fma_f32 v5, -v4, v3, v1
	v_cmp_ge_f32_e64 s[0:1], 0, v5
	v_add_u32_e32 v5, 1, v3
	s_nop 0
	v_cndmask_b32_e64 v4, v3, v4, s[0:1]
	v_fma_f32 v3, -v5, v3, v1
	v_cmp_lt_f32_e64 s[0:1], 0, v3
	s_nop 1
	v_cndmask_b32_e64 v3, v4, v5, s[0:1]
	v_mul_f32_e32 v4, 0x37800000, v3
	v_cndmask_b32_e32 v3, v3, v4, vcc
	v_mov_b32_e32 v4, 0x260
	v_cmp_class_f32_e32 vcc, v1, v4
	s_nop 1
	v_cndmask_b32_e32 v3, v3, v1, vcc
	v_div_scale_f32 v4, s[0:1], v3, v3, 1.0
	v_rcp_f32_e32 v5, v4
	s_nop 0
	v_fma_f32 v0, -v4, v5, 1.0
	v_fmac_f32_e32 v5, v0, v5
	v_div_scale_f32 v0, vcc, 1.0, v3, 1.0
	v_mul_f32_e32 v2, v0, v5
	v_fma_f32 v8, -v4, v2, v0
	v_fmac_f32_e32 v2, v8, v5
	v_fma_f32 v0, -v4, v2, v0
	v_div_fmas_f32 v0, v0, v5, v2
	v_div_fixup_f32 v2, v0, v3, 1.0
	v_mov_b32_e32 v42, v2
	v_mov_b32_e32 v43, v2
	ds_read_b32 v1, v7 offset:4608
	s_waitcnt lgkmcnt(0)
	v_add_f32_dpp v1, v1, v1 quad_perm:[1,0,3,2] row_mask:0xf bank_mask:0xf bound_ctrl:1
	s_nop 1
	v_add_f32_dpp v1, v1, v1 quad_perm:[2,3,0,1] row_mask:0xf bank_mask:0xf bound_ctrl:1
	s_nop 1
	v_add_f32_dpp v1, v1, v1 row_half_mirror row_mask:0xf bank_mask:0xf bound_ctrl:1
	s_nop 1
	v_add_f32_dpp v1, v1, v1 row_mirror row_mask:0xf bank_mask:0xf bound_ctrl:1
	s_nop 0
	v_readlane_b32 s1, v1, 16
	v_readlane_b32 s0, v1, 0
	s_nop 0
	v_mov_b32_e32 v3, s1
	v_readlane_b32 s1, v1, 48
	v_add_f32_e32 v3, s0, v3
	v_readlane_b32 s0, v1, 32
	v_mov_b32_e32 v1, s1
	s_nop 0
	v_add_f32_e32 v1, s0, v1
	v_add_f32_e32 v1, v3, v1
	v_mov_b32_e32 v3, 0x358637bd
	v_fmac_f32_e32 v3, 0x39800000, v1
	s_mov_b32 s0, 0xf800000
	v_mul_f32_e32 v1, 0x4f800000, v3
	v_cmp_gt_f32_e32 vcc, s0, v3
	s_nop 1
	v_cndmask_b32_e32 v1, v3, v1, vcc
	v_sqrt_f32_e32 v3, v1
	s_nop 0
	v_add_u32_e32 v4, -1, v3
	v_fma_f32 v5, -v4, v3, v1
	v_cmp_ge_f32_e64 s[0:1], 0, v5
	v_add_u32_e32 v5, 1, v3
	s_nop 0
	v_cndmask_b32_e64 v4, v3, v4, s[0:1]
	v_fma_f32 v3, -v5, v3, v1
	v_cmp_lt_f32_e64 s[0:1], 0, v3
	s_nop 1
	v_cndmask_b32_e64 v3, v4, v5, s[0:1]
	v_mul_f32_e32 v4, 0x37800000, v3
	v_cndmask_b32_e32 v3, v3, v4, vcc
	v_mov_b32_e32 v4, 0x260
	v_cmp_class_f32_e32 vcc, v1, v4
	s_nop 1
	v_cndmask_b32_e32 v3, v3, v1, vcc
	v_div_scale_f32 v4, s[0:1], v3, v3, 1.0
	v_rcp_f32_e32 v5, v4
	s_nop 0
	v_fma_f32 v0, -v4, v5, 1.0
	v_fmac_f32_e32 v5, v0, v5
	v_div_scale_f32 v0, vcc, 1.0, v3, 1.0
	v_mul_f32_e32 v2, v0, v5
	v_fma_f32 v8, -v4, v2, v0
	v_fmac_f32_e32 v2, v8, v5
	v_fma_f32 v0, -v4, v2, v0
	v_div_fmas_f32 v0, v0, v5, v2
	v_div_fixup_f32 v2, v0, v3, 1.0
	v_mov_b32_e32 v44, v2
	v_mov_b32_e32 v45, v2
	ds_read_b32 v1, v7 offset:4864
	s_waitcnt lgkmcnt(0)
; __device__ __forceinline__ int fresh_lane() { int l; asm volatile("v_mbcnt_lo_u32_b32 %0, -1, 0\n\tv_mbcnt_hi_u32_b32 %0, -1, %0" : "=v"(l)); return l; }
; __device__ __forceinline__ float wave_sum(float v) { v = dpp_add16(v); return (rdlane(v, 0) + rdlane(v, 16)) + (rdlane(v, 32) + rdlane(v, 48)); }
; __device__ __forceinline__ void p12_peer(Frame& F) {
;     ...
;       const int l2_ = fresh_lane(), lo2_ = 16 * (l2_ & 15) + 4 * (l2_ >> 4);
; #pragma unroll
;       for (int i = 0; i < 4; ++i) { const int t = F.gw + i * F.NGW;
;           const float rs = 1.0f / sqrtf(wave_sum(SSQ[i * 64 + l2_]) * (1.f / D_) + 1e-6f);
; _Pragma("nounroll")
;           for (int c0 = 0; c0 < 16; c0 += 8) {
; #pragma unroll
;               for (int c = c0; c < c0 + 8; ++c) { const size_t col = (size_t)t * D_ + (size_t)(unsigned)(256 * c + lo2_); const f32x4 gn = *(const f32x4*)(lnf + (256 * c + lo2_));
;                   const f32x4 o = *(const f32x4*)(F.out + col);
;                   *(f32x4*)(F.out + col) = (f32x4){o.x * rs * gn.x, o.y * rs * gn.y, o.z * rs * gn.z, o.w * rs * gn.w}; }
;               asm volatile("" ::: "memory"); } }
	v_add_f32_dpp v1, v1, v1 quad_perm:[1,0,3,2] row_mask:0xf bank_mask:0xf bound_ctrl:1
	s_nop 1
	v_add_f32_dpp v1, v1, v1 quad_perm:[2,3,0,1] row_mask:0xf bank_mask:0xf bound_ctrl:1
	s_nop 1
	v_add_f32_dpp v1, v1, v1 row_half_mirror row_mask:0xf bank_mask:0xf bound_ctrl:1
	s_nop 1
	v_add_f32_dpp v1, v1, v1 row_mirror row_mask:0xf bank_mask:0xf bound_ctrl:1
	s_nop 0
	v_readlane_b32 s1, v1, 16
	v_readlane_b32 s0, v1, 0
	s_nop 0
	v_mov_b32_e32 v3, s1
	v_readlane_b32 s1, v1, 48
	v_add_f32_e32 v3, s0, v3
	v_readlane_b32 s0, v1, 32
	v_mov_b32_e32 v1, s1
	s_nop 0
	v_add_f32_e32 v1, s0, v1
	v_add_f32_e32 v1, v3, v1
	v_mov_b32_e32 v3, 0x358637bd
	v_fmac_f32_e32 v3, 0x39800000, v1
	s_mov_b32 s0, 0xf800000
	v_mul_f32_e32 v1, 0x4f800000, v3
	v_cmp_gt_f32_e32 vcc, s0, v3
	s_nop 1
	v_cndmask_b32_e32 v1, v3, v1, vcc
	v_sqrt_f32_e32 v3, v1
	s_nop 0
	v_add_u32_e32 v4, -1, v3
	v_fma_f32 v5, -v4, v3, v1
	v_cmp_ge_f32_e64 s[0:1], 0, v5
	v_add_u32_e32 v5, 1, v3
	s_nop 0
	v_cndmask_b32_e64 v4, v3, v4, s[0:1]
	v_fma_f32 v3, -v5, v3, v1
	v_cmp_lt_f32_e64 s[0:1], 0, v3
	s_nop 1
	v_cndmask_b32_e64 v3, v4, v5, s[0:1]
	v_mul_f32_e32 v4, 0x37800000, v3
	v_cndmask_b32_e32 v3, v3, v4, vcc
	v_mov_b32_e32 v4, 0x260
	v_cmp_class_f32_e32 vcc, v1, v4
	s_nop 1
	v_cndmask_b32_e32 v3, v3, v1, vcc
	v_div_scale_f32 v4, s[0:1], v3, v3, 1.0
	v_rcp_f32_e32 v5, v4
	s_nop 0
	v_fma_f32 v0, -v4, v5, 1.0
	v_fmac_f32_e32 v5, v0, v5
	v_div_scale_f32 v0, vcc, 1.0, v3, 1.0
	v_mul_f32_e32 v2, v0, v5
	v_fma_f32 v8, -v4, v2, v0
	v_fmac_f32_e32 v2, v8, v5
	v_fma_f32 v0, -v4, v2, v0
	v_div_fmas_f32 v0, v0, v5, v2
	v_div_fixup_f32 v2, v0, v3, 1.0
	v_mov_b32_e32 v46, v2
	v_mov_b32_e32 v47, v2
	s_waitcnt vmcnt(31)
	v_pk_mul_f32 v[124:125], v[40:41], v[124:125]
	v_pk_mul_f32 v[126:127], v[40:41], v[126:127]
	v_pk_mul_f32 v[124:125], v[60:61], v[124:125]
	v_pk_mul_f32 v[126:127], v[62:63], v[126:127]
	global_store_dwordx4 v6, v[124:127], s[12:13] offset:0
	s_waitcnt vmcnt(31)
	v_pk_mul_f32 v[128:129], v[40:41], v[128:129]
	v_pk_mul_f32 v[130:131], v[40:41], v[130:131]
	v_pk_mul_f32 v[128:129], v[64:65], v[128:129]
	v_pk_mul_f32 v[130:131], v[66:67], v[130:131]
	global_store_dwordx4 v6, v[128:131], s[12:13] offset:1024
	s_waitcnt vmcnt(31)
	v_pk_mul_f32 v[132:133], v[40:41], v[132:133]
	v_pk_mul_f32 v[134:135], v[40:41], v[134:135]
	v_pk_mul_f32 v[132:133], v[68:69], v[132:133]
	v_pk_mul_f32 v[134:135], v[70:71], v[134:135]
	global_store_dwordx4 v6, v[132:135], s[12:13] offset:2048
	s_waitcnt vmcnt(31)
	v_pk_mul_f32 v[136:137], v[40:41], v[136:137]
	v_pk_mul_f32 v[138:139], v[40:41], v[138:139]
	v_pk_mul_f32 v[136:137], v[72:73], v[136:137]
	v_pk_mul_f32 v[138:139], v[74:75], v[138:139]
	global_store_dwordx4 v6, v[136:139], s[12:13] offset:3072
	s_waitcnt vmcnt(31)
	v_pk_mul_f32 v[140:141], v[40:41], v[140:141]
	v_pk_mul_f32 v[142:143], v[40:41], v[142:143]
	v_pk_mul_f32 v[140:141], v[76:77], v[140:141]
	v_pk_mul_f32 v[142:143], v[78:79], v[142:143]
	global_store_dwordx4 v10, v[140:143], s[12:13] offset:0
	s_waitcnt vmcnt(31)
	v_pk_mul_f32 v[144:145], v[40:41], v[144:145]
	v_pk_mul_f32 v[146:147], v[40:41], v[146:147]
	v_pk_mul_f32 v[144:145], v[80:81], v[144:145]
	v_pk_mul_f32 v[146:147], v[82:83], v[146:147]
	global_store_dwordx4 v10, v[144:147], s[12:13] offset:1024
	s_waitcnt vmcnt(31)
	v_pk_mul_f32 v[148:149], v[40:41], v[148:149]
	v_pk_mul_f32 v[150:151], v[40:41], v[150:151]
	v_pk_mul_f32 v[148:149], v[84:85], v[148:149]
	v_pk_mul_f32 v[150:151], v[86:87], v[150:151]
	global_store_dwordx4 v10, v[148:151], s[12:13] offset:2048
	s_waitcnt vmcnt(31)
	v_pk_mul_f32 v[152:153], v[40:41], v[152:153]
	v_pk_mul_f32 v[154:155], v[40:41], v[154:155]
	v_pk_mul_f32 v[152:153], v[88:89], v[152:153]
	v_pk_mul_f32 v[154:155], v[90:91], v[154:155]
	global_store_dwordx4 v10, v[152:155], s[12:13] offset:3072
	s_waitcnt vmcnt(31)
	v_pk_mul_f32 v[156:157], v[40:41], v[156:157]
	v_pk_mul_f32 v[158:159], v[40:41], v[158:159]
	v_pk_mul_f32 v[156:157], v[92:93], v[156:157]
	v_pk_mul_f32 v[158:159], v[94:95], v[158:159]
	global_store_dwordx4 v11, v[156:159], s[12:13] offset:0
	s_waitcnt vmcnt(31)
	v_pk_mul_f32 v[160:161], v[40:41], v[160:161]
	v_pk_mul_f32 v[162:163], v[40:41], v[162:163]
	v_pk_mul_f32 v[160:161], v[96:97], v[160:161]
	v_pk_mul_f32 v[162:163], v[98:99], v[162:163]
	global_store_dwordx4 v11, v[160:163], s[12:13] offset:1024
	s_waitcnt vmcnt(31)
	v_pk_mul_f32 v[164:165], v[40:41], v[164:165]
	v_pk_mul_f32 v[166:167], v[40:41], v[166:167]
	v_pk_mul_f32 v[164:165], v[100:101], v[164:165]
	v_pk_mul_f32 v[166:167], v[102:103], v[166:167]
	global_store_dwordx4 v11, v[164:167], s[12:13] offset:2048
	s_waitcnt vmcnt(31)
	v_pk_mul_f32 v[168:169], v[40:41], v[168:169]
	v_pk_mul_f32 v[170:171], v[40:41], v[170:171]
	v_pk_mul_f32 v[168:169], v[104:105], v[168:169]
	v_pk_mul_f32 v[170:171], v[106:107], v[170:171]
	global_store_dwordx4 v11, v[168:171], s[12:13] offset:3072
	s_waitcnt vmcnt(31)
	v_pk_mul_f32 v[172:173], v[40:41], v[172:173]
	v_pk_mul_f32 v[174:175], v[40:41], v[174:175]
	v_pk_mul_f32 v[172:173], v[108:109], v[172:173]
	v_pk_mul_f32 v[174:175], v[110:111], v[174:175]
	global_store_dwordx4 v12, v[172:175], s[12:13] offset:0
	s_waitcnt vmcnt(31)
	v_pk_mul_f32 v[176:177], v[40:41], v[176:177]
	v_pk_mul_f32 v[178:179], v[40:41], v[178:179]
	v_pk_mul_f32 v[176:177], v[112:113], v[176:177]
	v_pk_mul_f32 v[178:179], v[114:115], v[178:179]
	global_store_dwordx4 v12, v[176:179], s[12:13] offset:1024
	s_waitcnt vmcnt(31)
	v_pk_mul_f32 v[180:181], v[40:41], v[180:181]
	v_pk_mul_f32 v[182:183], v[40:41], v[182:183]
	v_pk_mul_f32 v[180:181], v[116:117], v[180:181]
	v_pk_mul_f32 v[182:183], v[118:119], v[182:183]
	global_store_dwordx4 v12, v[180:183], s[12:13] offset:2048
	s_waitcnt vmcnt(31)
; __device__ __forceinline__ int fresh_lane() { int l; asm volatile("v_mbcnt_lo_u32_b32 %0, -1, 0\n\tv_mbcnt_hi_u32_b32 %0, -1, %0" : "=v"(l)); return l; }
; __device__ __forceinline__ float wave_sum(float v) { v = dpp_add16(v); return (rdlane(v, 0) + rdlane(v, 16)) + (rdlane(v, 32) + rdlane(v, 48)); }
; __device__ __forceinline__ void p12_peer(Frame& F) {
;     ...
;       const int l2_ = fresh_lane(), lo2_ = 16 * (l2_ & 15) + 4 * (l2_ >> 4);
; #pragma unroll
;       for (int i = 0; i < 4; ++i) { const int t = F.gw + i * F.NGW;
;           const float rs = 1.0f / sqrtf(wave_sum(SSQ[i * 64 + l2_]) * (1.f / D_) + 1e-6f);
; _Pragma("nounroll")
;           for (int c0 = 0; c0 < 16; c0 += 8) {
; #pragma unroll
;               for (int c = c0; c < c0 + 8; ++c) { const size_t col = (size_t)t * D_ + (size_t)(unsigned)(256 * c + lo2_); const f32x4 gn = *(const f32x4*)(lnf + (256 * c + lo2_));
;                   const f32x4 o = *(const f32x4*)(F.out + col);
;                   *(f32x4*)(F.out + col) = (f32x4){o.x * rs * gn.x, o.y * rs * gn.y, o.z * rs * gn.z, o.w * rs * gn.w}; }
;               asm volatile("" ::: "memory"); } }
	v_pk_mul_f32 v[184:185], v[40:41], v[184:185]
	v_pk_mul_f32 v[186:187], v[40:41], v[186:187]
	v_pk_mul_f32 v[184:185], v[120:121], v[184:185]
	v_pk_mul_f32 v[186:187], v[122:123], v[186:187]
	global_store_dwordx4 v12, v[184:187], s[12:13] offset:3072
	s_nop 1
	global_load_dwordx4 v[124:127], v6, s[16:17] offset:0
	global_load_dwordx4 v[128:131], v6, s[16:17] offset:1024
	global_load_dwordx4 v[132:135], v6, s[16:17] offset:2048
	global_load_dwordx4 v[136:139], v6, s[16:17] offset:3072
	global_load_dwordx4 v[140:143], v10, s[16:17] offset:0
	global_load_dwordx4 v[144:147], v10, s[16:17] offset:1024
	global_load_dwordx4 v[148:151], v10, s[16:17] offset:2048
	global_load_dwordx4 v[152:155], v10, s[16:17] offset:3072
	global_load_dwordx4 v[156:159], v11, s[16:17] offset:0
	global_load_dwordx4 v[160:163], v11, s[16:17] offset:1024
	global_load_dwordx4 v[164:167], v11, s[16:17] offset:2048
	global_load_dwordx4 v[168:171], v11, s[16:17] offset:3072
	global_load_dwordx4 v[172:175], v12, s[16:17] offset:0
	global_load_dwordx4 v[176:179], v12, s[16:17] offset:1024
	global_load_dwordx4 v[180:183], v12, s[16:17] offset:2048
	global_load_dwordx4 v[184:187], v12, s[16:17] offset:3072
	s_waitcnt vmcnt(47)
	v_pk_mul_f32 v[188:189], v[42:43], v[188:189]
	v_pk_mul_f32 v[190:191], v[42:43], v[190:191]
	v_pk_mul_f32 v[188:189], v[60:61], v[188:189]
	v_pk_mul_f32 v[190:191], v[62:63], v[190:191]
	global_store_dwordx4 v6, v[188:191], s[14:15] offset:0
	s_waitcnt vmcnt(47)
	v_pk_mul_f32 v[192:193], v[42:43], v[192:193]
	v_pk_mul_f32 v[194:195], v[42:43], v[194:195]
	v_pk_mul_f32 v[192:193], v[64:65], v[192:193]
	v_pk_mul_f32 v[194:195], v[66:67], v[194:195]
	global_store_dwordx4 v6, v[192:195], s[14:15] offset:1024
	s_waitcnt vmcnt(47)
	v_pk_mul_f32 v[196:197], v[42:43], v[196:197]
	v_pk_mul_f32 v[198:199], v[42:43], v[198:199]
	v_pk_mul_f32 v[196:197], v[68:69], v[196:197]
	v_pk_mul_f32 v[198:199], v[70:71], v[198:199]
	global_store_dwordx4 v6, v[196:199], s[14:15] offset:2048
	s_waitcnt vmcnt(47)
	v_pk_mul_f32 v[200:201], v[42:43], v[200:201]
	v_pk_mul_f32 v[202:203], v[42:43], v[202:203]
	v_pk_mul_f32 v[200:201], v[72:73], v[200:201]
	v_pk_mul_f32 v[202:203], v[74:75], v[202:203]
	global_store_dwordx4 v6, v[200:203], s[14:15] offset:3072
	s_waitcnt vmcnt(47)
	v_pk_mul_f32 v[204:205], v[42:43], v[204:205]
	v_pk_mul_f32 v[206:207], v[42:43], v[206:207]
	v_pk_mul_f32 v[204:205], v[76:77], v[204:205]
	v_pk_mul_f32 v[206:207], v[78:79], v[206:207]
	global_store_dwordx4 v10, v[204:207], s[14:15] offset:0
	s_waitcnt vmcnt(47)
	v_pk_mul_f32 v[208:209], v[42:43], v[208:209]
	v_pk_mul_f32 v[210:211], v[42:43], v[210:211]
	v_pk_mul_f32 v[208:209], v[80:81], v[208:209]
	v_pk_mul_f32 v[210:211], v[82:83], v[210:211]
	global_store_dwordx4 v10, v[208:211], s[14:15] offset:1024
	s_waitcnt vmcnt(47)
	v_pk_mul_f32 v[212:213], v[42:43], v[212:213]
	v_pk_mul_f32 v[214:215], v[42:43], v[214:215]
	v_pk_mul_f32 v[212:213], v[84:85], v[212:213]
	v_pk_mul_f32 v[214:215], v[86:87], v[214:215]
	global_store_dwordx4 v10, v[212:215], s[14:15] offset:2048
	s_waitcnt vmcnt(47)
	v_pk_mul_f32 v[216:217], v[42:43], v[216:217]
	v_pk_mul_f32 v[218:219], v[42:43], v[218:219]
	v_pk_mul_f32 v[216:217], v[88:89], v[216:217]
	v_pk_mul_f32 v[218:219], v[90:91], v[218:219]
	global_store_dwordx4 v10, v[216:219], s[14:15] offset:3072
	s_waitcnt vmcnt(47)
	v_pk_mul_f32 v[220:221], v[42:43], v[220:221]
	v_pk_mul_f32 v[222:223], v[42:43], v[222:223]
	v_pk_mul_f32 v[220:221], v[92:93], v[220:221]
	v_pk_mul_f32 v[222:223], v[94:95], v[222:223]
	global_store_dwordx4 v11, v[220:223], s[14:15] offset:0
	s_waitcnt vmcnt(47)
	v_pk_mul_f32 v[224:225], v[42:43], v[224:225]
	v_pk_mul_f32 v[226:227], v[42:43], v[226:227]
	v_pk_mul_f32 v[224:225], v[96:97], v[224:225]
	v_pk_mul_f32 v[226:227], v[98:99], v[226:227]
	global_store_dwordx4 v11, v[224:227], s[14:15] offset:1024
	s_waitcnt vmcnt(47)
	v_pk_mul_f32 v[228:229], v[42:43], v[228:229]
	v_pk_mul_f32 v[230:231], v[42:43], v[230:231]
	v_pk_mul_f32 v[228:229], v[100:101], v[228:229]
	v_pk_mul_f32 v[230:231], v[102:103], v[230:231]
	global_store_dwordx4 v11, v[228:231], s[14:15] offset:2048
	s_waitcnt vmcnt(47)
	v_pk_mul_f32 v[232:233], v[42:43], v[232:233]
	v_pk_mul_f32 v[234:235], v[42:43], v[234:235]
	v_pk_mul_f32 v[232:233], v[104:105], v[232:233]
	v_pk_mul_f32 v[234:235], v[106:107], v[234:235]
	global_store_dwordx4 v11, v[232:235], s[14:15] offset:3072
	s_waitcnt vmcnt(47)
	v_pk_mul_f32 v[236:237], v[42:43], v[236:237]
	v_pk_mul_f32 v[238:239], v[42:43], v[238:239]
	v_pk_mul_f32 v[236:237], v[108:109], v[236:237]
	v_pk_mul_f32 v[238:239], v[110:111], v[238:239]
	global_store_dwordx4 v12, v[236:239], s[14:15] offset:0
	s_waitcnt vmcnt(47)
	v_pk_mul_f32 v[240:241], v[42:43], v[240:241]
	v_pk_mul_f32 v[242:243], v[42:43], v[242:243]
	v_pk_mul_f32 v[240:241], v[112:113], v[240:241]
	v_pk_mul_f32 v[242:243], v[114:115], v[242:243]
	global_store_dwordx4 v12, v[240:243], s[14:15] offset:1024
	s_waitcnt vmcnt(47)
	v_pk_mul_f32 v[244:245], v[42:43], v[244:245]
	v_pk_mul_f32 v[246:247], v[42:43], v[246:247]
	v_pk_mul_f32 v[244:245], v[116:117], v[244:245]
	v_pk_mul_f32 v[246:247], v[118:119], v[246:247]
	global_store_dwordx4 v12, v[244:247], s[14:15] offset:2048
	s_waitcnt vmcnt(47)
; __device__ __forceinline__ int fresh_lane() { int l; asm volatile("v_mbcnt_lo_u32_b32 %0, -1, 0\n\tv_mbcnt_hi_u32_b32 %0, -1, %0" : "=v"(l)); return l; }
; __device__ __forceinline__ float wave_sum(float v) { v = dpp_add16(v); return (rdlane(v, 0) + rdlane(v, 16)) + (rdlane(v, 32) + rdlane(v, 48)); }
; __device__ __forceinline__ void p12_peer(Frame& F) {
;     ...
;       const int l2_ = fresh_lane(), lo2_ = 16 * (l2_ & 15) + 4 * (l2_ >> 4);
; #pragma unroll
;       for (int i = 0; i < 4; ++i) { const int t = F.gw + i * F.NGW;
;           const float rs = 1.0f / sqrtf(wave_sum(SSQ[i * 64 + l2_]) * (1.f / D_) + 1e-6f);
; _Pragma("nounroll")
;           for (int c0 = 0; c0 < 16; c0 += 8) {
; #pragma unroll
;               for (int c = c0; c < c0 + 8; ++c) { const size_t col = (size_t)t * D_ + (size_t)(unsigned)(256 * c + lo2_); const f32x4 gn = *(const f32x4*)(lnf + (256 * c + lo2_));
;                   const f32x4 o = *(const f32x4*)(F.out + col);
;                   *(f32x4*)(F.out + col) = (f32x4){o.x * rs * gn.x, o.y * rs * gn.y, o.z * rs * gn.z, o.w * rs * gn.w}; }
;               asm volatile("" ::: "memory"); } }
	v_pk_mul_f32 v[248:249], v[42:43], v[248:249]
	v_pk_mul_f32 v[250:251], v[42:43], v[250:251]
	v_pk_mul_f32 v[248:249], v[120:121], v[248:249]
	v_pk_mul_f32 v[250:251], v[122:123], v[250:251]
	global_store_dwordx4 v12, v[248:251], s[14:15] offset:3072
	s_nop 1
	global_load_dwordx4 v[188:191], v6, s[18:19] offset:0
	global_load_dwordx4 v[192:195], v6, s[18:19] offset:1024
	global_load_dwordx4 v[196:199], v6, s[18:19] offset:2048
	global_load_dwordx4 v[200:203], v6, s[18:19] offset:3072
	global_load_dwordx4 v[204:207], v10, s[18:19] offset:0
	global_load_dwordx4 v[208:211], v10, s[18:19] offset:1024
	global_load_dwordx4 v[212:215], v10, s[18:19] offset:2048
	global_load_dwordx4 v[216:219], v10, s[18:19] offset:3072
	global_load_dwordx4 v[220:223], v11, s[18:19] offset:0
	global_load_dwordx4 v[224:227], v11, s[18:19] offset:1024
	global_load_dwordx4 v[228:231], v11, s[18:19] offset:2048
	global_load_dwordx4 v[232:235], v11, s[18:19] offset:3072
	global_load_dwordx4 v[236:239], v12, s[18:19] offset:0
	global_load_dwordx4 v[240:243], v12, s[18:19] offset:1024
	global_load_dwordx4 v[244:247], v12, s[18:19] offset:2048
	global_load_dwordx4 v[248:251], v12, s[18:19] offset:3072
	s_waitcnt vmcnt(47)
	v_pk_mul_f32 v[124:125], v[44:45], v[124:125]
	v_pk_mul_f32 v[126:127], v[44:45], v[126:127]
	v_pk_mul_f32 v[124:125], v[60:61], v[124:125]
	v_pk_mul_f32 v[126:127], v[62:63], v[126:127]
	global_store_dwordx4 v6, v[124:127], s[16:17] offset:0
	s_waitcnt vmcnt(47)
	v_pk_mul_f32 v[128:129], v[44:45], v[128:129]
	v_pk_mul_f32 v[130:131], v[44:45], v[130:131]
	v_pk_mul_f32 v[128:129], v[64:65], v[128:129]
	v_pk_mul_f32 v[130:131], v[66:67], v[130:131]
	global_store_dwordx4 v6, v[128:131], s[16:17] offset:1024
	s_waitcnt vmcnt(47)
	v_pk_mul_f32 v[132:133], v[44:45], v[132:133]
	v_pk_mul_f32 v[134:135], v[44:45], v[134:135]
	v_pk_mul_f32 v[132:133], v[68:69], v[132:133]
	v_pk_mul_f32 v[134:135], v[70:71], v[134:135]
	global_store_dwordx4 v6, v[132:135], s[16:17] offset:2048
	s_waitcnt vmcnt(47)
	v_pk_mul_f32 v[136:137], v[44:45], v[136:137]
	v_pk_mul_f32 v[138:139], v[44:45], v[138:139]
	v_pk_mul_f32 v[136:137], v[72:73], v[136:137]
	v_pk_mul_f32 v[138:139], v[74:75], v[138:139]
	global_store_dwordx4 v6, v[136:139], s[16:17] offset:3072
	s_waitcnt vmcnt(47)
	v_pk_mul_f32 v[140:141], v[44:45], v[140:141]
	v_pk_mul_f32 v[142:143], v[44:45], v[142:143]
	v_pk_mul_f32 v[140:141], v[76:77], v[140:141]
	v_pk_mul_f32 v[142:143], v[78:79], v[142:143]
	global_store_dwordx4 v10, v[140:143], s[16:17] offset:0
	s_waitcnt vmcnt(47)
	v_pk_mul_f32 v[144:145], v[44:45], v[144:145]
	v_pk_mul_f32 v[146:147], v[44:45], v[146:147]
	v_pk_mul_f32 v[144:145], v[80:81], v[144:145]
	v_pk_mul_f32 v[146:147], v[82:83], v[146:147]
	global_store_dwordx4 v10, v[144:147], s[16:17] offset:1024
	s_waitcnt vmcnt(47)
	v_pk_mul_f32 v[148:149], v[44:45], v[148:149]
	v_pk_mul_f32 v[150:151], v[44:45], v[150:151]
	v_pk_mul_f32 v[148:149], v[84:85], v[148:149]
	v_pk_mul_f32 v[150:151], v[86:87], v[150:151]
	global_store_dwordx4 v10, v[148:151], s[16:17] offset:2048
	s_waitcnt vmcnt(47)
	v_pk_mul_f32 v[152:153], v[44:45], v[152:153]
	v_pk_mul_f32 v[154:155], v[44:45], v[154:155]
	v_pk_mul_f32 v[152:153], v[88:89], v[152:153]
	v_pk_mul_f32 v[154:155], v[90:91], v[154:155]
	global_store_dwordx4 v10, v[152:155], s[16:17] offset:3072
	s_waitcnt vmcnt(47)
	v_pk_mul_f32 v[156:157], v[44:45], v[156:157]
	v_pk_mul_f32 v[158:159], v[44:45], v[158:159]
	v_pk_mul_f32 v[156:157], v[92:93], v[156:157]
	v_pk_mul_f32 v[158:159], v[94:95], v[158:159]
	global_store_dwordx4 v11, v[156:159], s[16:17] offset:0
	s_waitcnt vmcnt(47)
	v_pk_mul_f32 v[160:161], v[44:45], v[160:161]
	v_pk_mul_f32 v[162:163], v[44:45], v[162:163]
	v_pk_mul_f32 v[160:161], v[96:97], v[160:161]
	v_pk_mul_f32 v[162:163], v[98:99], v[162:163]
	global_store_dwordx4 v11, v[160:163], s[16:17] offset:1024
	s_waitcnt vmcnt(47)
	v_pk_mul_f32 v[164:165], v[44:45], v[164:165]
	v_pk_mul_f32 v[166:167], v[44:45], v[166:167]
	v_pk_mul_f32 v[164:165], v[100:101], v[164:165]
	v_pk_mul_f32 v[166:167], v[102:103], v[166:167]
	global_store_dwordx4 v11, v[164:167], s[16:17] offset:2048
	s_waitcnt vmcnt(47)
	v_pk_mul_f32 v[168:169], v[44:45], v[168:169]
	v_pk_mul_f32 v[170:171], v[44:45], v[170:171]
	v_pk_mul_f32 v[168:169], v[104:105], v[168:169]
	v_pk_mul_f32 v[170:171], v[106:107], v[170:171]
	global_store_dwordx4 v11, v[168:171], s[16:17] offset:3072
	s_waitcnt vmcnt(47)
	v_pk_mul_f32 v[172:173], v[44:45], v[172:173]
	v_pk_mul_f32 v[174:175], v[44:45], v[174:175]
	v_pk_mul_f32 v[172:173], v[108:109], v[172:173]
	v_pk_mul_f32 v[174:175], v[110:111], v[174:175]
	global_store_dwordx4 v12, v[172:175], s[16:17] offset:0
	s_waitcnt vmcnt(47)
	v_pk_mul_f32 v[176:177], v[44:45], v[176:177]
	v_pk_mul_f32 v[178:179], v[44:45], v[178:179]
	v_pk_mul_f32 v[176:177], v[112:113], v[176:177]
	v_pk_mul_f32 v[178:179], v[114:115], v[178:179]
	global_store_dwordx4 v12, v[176:179], s[16:17] offset:1024
	s_waitcnt vmcnt(47)
; __device__ __forceinline__ int fresh_lane() { int l; asm volatile("v_mbcnt_lo_u32_b32 %0, -1, 0\n\tv_mbcnt_hi_u32_b32 %0, -1, %0" : "=v"(l)); return l; }
; __device__ __forceinline__ float wave_sum(float v) { v = dpp_add16(v); return (rdlane(v, 0) + rdlane(v, 16)) + (rdlane(v, 32) + rdlane(v, 48)); }
; __device__ __forceinline__ void p12_peer(Frame& F) {
;     ...
;       const int l2_ = fresh_lane(), lo2_ = 16 * (l2_ & 15) + 4 * (l2_ >> 4);
; #pragma unroll
;       for (int i = 0; i < 4; ++i) { const int t = F.gw + i * F.NGW;
;           const float rs = 1.0f / sqrtf(wave_sum(SSQ[i * 64 + l2_]) * (1.f / D_) + 1e-6f);
; _Pragma("nounroll")
;           for (int c0 = 0; c0 < 16; c0 += 8) {
; #pragma unroll
;               for (int c = c0; c < c0 + 8; ++c) { const size_t col = (size_t)t * D_ + (size_t)(unsigned)(256 * c + lo2_); const f32x4 gn = *(const f32x4*)(lnf + (256 * c + lo2_));
;                   const f32x4 o = *(const f32x4*)(F.out + col);
;                   *(f32x4*)(F.out + col) = (f32x4){o.x * rs * gn.x, o.y * rs * gn.y, o.z * rs * gn.z, o.w * rs * gn.w}; }
;               asm volatile("" ::: "memory"); } }
	v_pk_mul_f32 v[180:181], v[44:45], v[180:181]
	v_pk_mul_f32 v[182:183], v[44:45], v[182:183]
	v_pk_mul_f32 v[180:181], v[116:117], v[180:181]
	v_pk_mul_f32 v[182:183], v[118:119], v[182:183]
	global_store_dwordx4 v12, v[180:183], s[16:17] offset:2048
	s_waitcnt vmcnt(47)
	v_pk_mul_f32 v[184:185], v[44:45], v[184:185]
	v_pk_mul_f32 v[186:187], v[44:45], v[186:187]
	v_pk_mul_f32 v[184:185], v[120:121], v[184:185]
	v_pk_mul_f32 v[186:187], v[122:123], v[186:187]
	global_store_dwordx4 v12, v[184:187], s[16:17] offset:3072
	s_waitcnt vmcnt(31)
	v_pk_mul_f32 v[188:189], v[46:47], v[188:189]
	v_pk_mul_f32 v[190:191], v[46:47], v[190:191]
	v_pk_mul_f32 v[188:189], v[60:61], v[188:189]
	v_pk_mul_f32 v[190:191], v[62:63], v[190:191]
	global_store_dwordx4 v6, v[188:191], s[18:19] offset:0
	s_waitcnt vmcnt(31)
	v_pk_mul_f32 v[192:193], v[46:47], v[192:193]
	v_pk_mul_f32 v[194:195], v[46:47], v[194:195]
	v_pk_mul_f32 v[192:193], v[64:65], v[192:193]
	v_pk_mul_f32 v[194:195], v[66:67], v[194:195]
	global_store_dwordx4 v6, v[192:195], s[18:19] offset:1024
	s_waitcnt vmcnt(31)
	v_pk_mul_f32 v[196:197], v[46:47], v[196:197]
	v_pk_mul_f32 v[198:199], v[46:47], v[198:199]
	v_pk_mul_f32 v[196:197], v[68:69], v[196:197]
	v_pk_mul_f32 v[198:199], v[70:71], v[198:199]
	global_store_dwordx4 v6, v[196:199], s[18:19] offset:2048
	s_waitcnt vmcnt(31)
	v_pk_mul_f32 v[200:201], v[46:47], v[200:201]
	v_pk_mul_f32 v[202:203], v[46:47], v[202:203]
	v_pk_mul_f32 v[200:201], v[72:73], v[200:201]
	v_pk_mul_f32 v[202:203], v[74:75], v[202:203]
	global_store_dwordx4 v6, v[200:203], s[18:19] offset:3072
	s_waitcnt vmcnt(31)
	v_pk_mul_f32 v[204:205], v[46:47], v[204:205]
	v_pk_mul_f32 v[206:207], v[46:47], v[206:207]
	v_pk_mul_f32 v[204:205], v[76:77], v[204:205]
	v_pk_mul_f32 v[206:207], v[78:79], v[206:207]
	global_store_dwordx4 v10, v[204:207], s[18:19] offset:0
	s_waitcnt vmcnt(31)
	v_pk_mul_f32 v[208:209], v[46:47], v[208:209]
	v_pk_mul_f32 v[210:211], v[46:47], v[210:211]
	v_pk_mul_f32 v[208:209], v[80:81], v[208:209]
	v_pk_mul_f32 v[210:211], v[82:83], v[210:211]
	global_store_dwordx4 v10, v[208:211], s[18:19] offset:1024
	s_waitcnt vmcnt(31)
	v_pk_mul_f32 v[212:213], v[46:47], v[212:213]
	v_pk_mul_f32 v[214:215], v[46:47], v[214:215]
	v_pk_mul_f32 v[212:213], v[84:85], v[212:213]
	v_pk_mul_f32 v[214:215], v[86:87], v[214:215]
	global_store_dwordx4 v10, v[212:215], s[18:19] offset:2048
	s_waitcnt vmcnt(31)
	v_pk_mul_f32 v[216:217], v[46:47], v[216:217]
	v_pk_mul_f32 v[218:219], v[46:47], v[218:219]
	v_pk_mul_f32 v[216:217], v[88:89], v[216:217]
	v_pk_mul_f32 v[218:219], v[90:91], v[218:219]
	global_store_dwordx4 v10, v[216:219], s[18:19] offset:3072
	s_waitcnt vmcnt(31)
	v_pk_mul_f32 v[220:221], v[46:47], v[220:221]
	v_pk_mul_f32 v[222:223], v[46:47], v[222:223]
	v_pk_mul_f32 v[220:221], v[92:93], v[220:221]
	v_pk_mul_f32 v[222:223], v[94:95], v[222:223]
	global_store_dwordx4 v11, v[220:223], s[18:19] offset:0
	s_waitcnt vmcnt(31)
	v_pk_mul_f32 v[224:225], v[46:47], v[224:225]
	v_pk_mul_f32 v[226:227], v[46:47], v[226:227]
	v_pk_mul_f32 v[224:225], v[96:97], v[224:225]
	v_pk_mul_f32 v[226:227], v[98:99], v[226:227]
	global_store_dwordx4 v11, v[224:227], s[18:19] offset:1024
	s_waitcnt vmcnt(31)
	v_pk_mul_f32 v[228:229], v[46:47], v[228:229]
	v_pk_mul_f32 v[230:231], v[46:47], v[230:231]
	v_pk_mul_f32 v[228:229], v[100:101], v[228:229]
	v_pk_mul_f32 v[230:231], v[102:103], v[230:231]
	global_store_dwordx4 v11, v[228:231], s[18:19] offset:2048
	s_waitcnt vmcnt(31)
	v_pk_mul_f32 v[232:233], v[46:47], v[232:233]
	v_pk_mul_f32 v[234:235], v[46:47], v[234:235]
	v_pk_mul_f32 v[232:233], v[104:105], v[232:233]
	v_pk_mul_f32 v[234:235], v[106:107], v[234:235]
	global_store_dwordx4 v11, v[232:235], s[18:19] offset:3072
	s_waitcnt vmcnt(31)
	v_pk_mul_f32 v[236:237], v[46:47], v[236:237]
	v_pk_mul_f32 v[238:239], v[46:47], v[238:239]
	v_pk_mul_f32 v[236:237], v[108:109], v[236:237]
	v_pk_mul_f32 v[238:239], v[110:111], v[238:239]
	global_store_dwordx4 v12, v[236:239], s[18:19] offset:0
	s_waitcnt vmcnt(31)
	v_pk_mul_f32 v[240:241], v[46:47], v[240:241]
	v_pk_mul_f32 v[242:243], v[46:47], v[242:243]
	v_pk_mul_f32 v[240:241], v[112:113], v[240:241]
	v_pk_mul_f32 v[242:243], v[114:115], v[242:243]
	global_store_dwordx4 v12, v[240:243], s[18:19] offset:1024
	s_waitcnt vmcnt(31)
	v_pk_mul_f32 v[244:245], v[46:47], v[244:245]
	v_pk_mul_f32 v[246:247], v[46:47], v[246:247]
	v_pk_mul_f32 v[244:245], v[116:117], v[244:245]
	v_pk_mul_f32 v[246:247], v[118:119], v[246:247]
	global_store_dwordx4 v12, v[244:247], s[18:19] offset:2048
	s_waitcnt vmcnt(31)
	v_pk_mul_f32 v[248:249], v[46:47], v[248:249]
	v_pk_mul_f32 v[250:251], v[46:47], v[250:251]
	v_pk_mul_f32 v[248:249], v[120:121], v[248:249]
	v_pk_mul_f32 v[250:251], v[122:123], v[250:251]
	global_store_dwordx4 v12, v[248:251], s[18:19] offset:3072
